# hand-scheduled FFN-in SwiGLU->fp8 epilogue (bit-exact, no nop stalls, packed f32 muls, 32-bit store offsets) + DSA pass-1 tile body unrolled/overlapped + counted vmcnt in pass-1 tile loop
# speedup vs baseline: 1.0194x; 1.0194x over previous
.LBB0_497:
	s_or_b64 exec, exec, s[0:1]
	s_mul_i32 s0, s44, 0x1200000
	s_mul_hi_i32 s1, s44, 0x1200000
	s_add_u32 s0, s74, s0
	s_addc_u32 s1, s75, s1
	s_add_i32 s12, 0, 0x23400
	v_ashrrev_i32_e32 v54, 4, v42
	v_mov_b32_e32 v0, s12
	s_lshl_b32 s49, s30, 6
	v_readlane_b32 s13, v252, 19
	v_and_b32_e32 v232, 15, v42
	s_waitcnt lgkmcnt(0)
	s_barrier
	ds_read_b128 v[6:9], v0
	ds_read_b128 v[2:5], v0 offset:16
	s_or_b32 s12, s49, s13
	v_mov_b32_e32 v0, v54
	v_or_b32_e32 v44, s12, v232
	v_mov_b64_e32 v[10:11], s[0:1]
	v_lshlrev_b32_e32 v12, 3, v0
	v_mad_i64_i32 v[10:11], s[0:1], v44, s2, v[10:11]
	v_ashrrev_i32_e32 v13, 31, v12
	v_lshl_add_u64 v[38:39], v[12:13], 1, v[10:11]
	global_load_dwordx4 v[10:13], v[38:39], off offset:2048
	global_load_dwordx4 v[14:17], v[38:39], off offset:2112
	v_ashrrev_i32_e32 v45, 31, v44
	v_lshlrev_b64 v[18:19], 9, v[44:45]
	v_lshl_add_u64 v[18:19], s[42:43], 0, v[18:19]
	global_load_dwordx2 v[50:51], v[18:19], off offset:384
	v_ashrrev_i32_e32 v233, 3, v42
	v_readlane_b32 s12, v251, 50
	s_add_u32 s0, s42, 0x100
	s_addc_u32 s1, s43, 0
	v_add_u32_e32 v46, s12, v233
	v_ashrrev_i32_e32 v47, 31, v46
	v_lshlrev_b64 v[46:47], 9, v[46:47]
	s_movk_i32 s12, 0x70
	s_mov_b64 s[16:17], 0x8000
	s_add_i32 s30, s30, 2
	s_ashr_i32 s50, s30, 1
	v_ashrrev_i32_e32 v43, 31, v42
	s_waitcnt vmcnt(2)
	v_lshlrev_b32_e32 v0, 16, v10
	v_and_b32_e32 v10, 0xffff0000, v10
	v_lshlrev_b32_e32 v18, 16, v11
	v_and_b32_e32 v11, 0xffff0000, v11
	v_lshlrev_b32_e32 v19, 16, v12
	v_and_b32_e32 v12, 0xffff0000, v12
	v_mul_f32_e32 v10, v10, v10
	v_mul_f32_e32 v11, v11, v11
	v_lshlrev_b32_e32 v20, 16, v13
	v_and_b32_e32 v13, 0xffff0000, v13
	v_mul_f32_e32 v12, v12, v12
	v_fmac_f32_e32 v10, v0, v0
	v_fmac_f32_e32 v11, v18, v18
	s_waitcnt vmcnt(1)
	v_lshlrev_b32_e32 v21, 16, v14
	v_and_b32_e32 v14, 0xffff0000, v14
	v_mul_f32_e32 v13, v13, v13
	v_fmac_f32_e32 v12, v19, v19
	v_add_f32_e32 v0, v10, v11
	v_lshlrev_b32_e32 v22, 16, v15
	v_and_b32_e32 v15, 0xffff0000, v15
	v_mul_f32_e32 v14, v14, v14
	v_fmac_f32_e32 v13, v20, v20
	v_add_f32_e32 v0, v12, v0
	v_lshlrev_b32_e32 v23, 16, v16
	v_and_b32_e32 v16, 0xffff0000, v16
	v_mul_f32_e32 v15, v15, v15
	v_fmac_f32_e32 v14, v21, v21
	v_add_f32_e32 v0, v13, v0
	v_lshlrev_b32_e32 v24, 16, v17
	v_and_b32_e32 v17, 0xffff0000, v17
	v_mul_f32_e32 v16, v16, v16
	v_fmac_f32_e32 v15, v22, v22
	v_add_f32_e32 v0, v14, v0
	v_mul_f32_e32 v17, v17, v17
	v_fmac_f32_e32 v16, v23, v23
	v_add_f32_e32 v0, v15, v0
	v_fmac_f32_e32 v17, v24, v24
	v_add_f32_e32 v0, v16, v0
	v_add_f32_e32 v0, v17, v0
	v_mov_b32_e32 v10, v0
	s_nop 1
	v_permlane16_swap_b32_e32 v0, v10
	v_add_f32_e32 v56, v0, v10
	v_mov_b32_e32 v57, v56
	global_load_dwordx4 v[10:13], v[38:39], off offset:2176
	global_load_dwordx4 v[14:17], v[38:39], off offset:2240
	v_permlane32_swap_b32_e32 v56, v57
	s_waitcnt vmcnt(1)
	v_lshlrev_b32_e32 v0, 16, v10
	v_and_b32_e32 v10, 0xffff0000, v10
	v_lshlrev_b32_e32 v18, 16, v11
	v_and_b32_e32 v11, 0xffff0000, v11
	v_lshlrev_b32_e32 v19, 16, v12
	v_and_b32_e32 v12, 0xffff0000, v12
	v_mul_f32_e32 v10, v10, v10
	v_mul_f32_e32 v11, v11, v11
	v_lshlrev_b32_e32 v20, 16, v13
	v_and_b32_e32 v13, 0xffff0000, v13
	v_mul_f32_e32 v12, v12, v12
	v_fmac_f32_e32 v10, v0, v0
	v_fmac_f32_e32 v11, v18, v18
	s_waitcnt vmcnt(0)
	v_lshlrev_b32_e32 v21, 16, v14
	v_and_b32_e32 v14, 0xffff0000, v14
	v_mul_f32_e32 v13, v13, v13
	v_fmac_f32_e32 v12, v19, v19
	v_add_f32_e32 v0, v10, v11
	v_lshlrev_b32_e32 v22, 16, v15
	v_and_b32_e32 v15, 0xffff0000, v15
	v_mul_f32_e32 v14, v14, v14
	v_fmac_f32_e32 v13, v20, v20
	v_add_f32_e32 v0, v12, v0
	v_lshlrev_b32_e32 v23, 16, v16
	v_and_b32_e32 v16, 0xffff0000, v16
	v_mul_f32_e32 v15, v15, v15
	v_fmac_f32_e32 v14, v21, v21
	v_add_f32_e32 v0, v13, v0
	v_lshlrev_b32_e32 v24, 16, v17
	v_and_b32_e32 v17, 0xffff0000, v17
	v_mul_f32_e32 v16, v16, v16
	v_fmac_f32_e32 v15, v22, v22
	v_add_f32_e32 v0, v14, v0
	v_mul_f32_e32 v17, v17, v17
	v_fmac_f32_e32 v16, v23, v23
	v_add_f32_e32 v0, v15, v0
	v_fmac_f32_e32 v17, v24, v24
	v_add_f32_e32 v0, v16, v0
	v_add_f32_e32 v0, v17, v0
	v_mov_b32_e32 v10, v0
	s_nop 1
	v_permlane16_swap_b32_e32 v0, v10
	v_add_f32_e32 v58, v0, v10
	v_mov_b32_e32 v59, v58
	global_load_dwordx4 v[10:13], v[38:39], off offset:2304
	global_load_dwordx4 v[14:17], v[38:39], off offset:2368
	v_permlane32_swap_b32_e32 v58, v59
	s_waitcnt vmcnt(1)
	v_lshlrev_b32_e32 v0, 16, v10
	v_and_b32_e32 v10, 0xffff0000, v10
	v_lshlrev_b32_e32 v18, 16, v11
	v_and_b32_e32 v11, 0xffff0000, v11
	v_lshlrev_b32_e32 v19, 16, v12
	v_and_b32_e32 v12, 0xffff0000, v12
	v_mul_f32_e32 v10, v10, v10
	v_mul_f32_e32 v11, v11, v11
	v_lshlrev_b32_e32 v20, 16, v13
	v_and_b32_e32 v13, 0xffff0000, v13
	v_mul_f32_e32 v12, v12, v12
	v_fmac_f32_e32 v10, v0, v0
	v_fmac_f32_e32 v11, v18, v18
	s_waitcnt vmcnt(0)
	v_lshlrev_b32_e32 v21, 16, v14
	v_and_b32_e32 v14, 0xffff0000, v14
	v_mul_f32_e32 v13, v13, v13
	v_fmac_f32_e32 v12, v19, v19
	v_add_f32_e32 v0, v10, v11
	v_lshlrev_b32_e32 v22, 16, v15
	v_and_b32_e32 v15, 0xffff0000, v15
	v_mul_f32_e32 v14, v14, v14
	v_fmac_f32_e32 v13, v20, v20
	v_add_f32_e32 v0, v12, v0
	v_lshlrev_b32_e32 v23, 16, v16
	v_and_b32_e32 v16, 0xffff0000, v16
	v_mul_f32_e32 v15, v15, v15
	v_fmac_f32_e32 v14, v21, v21
	v_add_f32_e32 v0, v13, v0
	v_lshlrev_b32_e32 v24, 16, v17
	v_and_b32_e32 v17, 0xffff0000, v17
	v_mul_f32_e32 v16, v16, v16
	v_fmac_f32_e32 v15, v22, v22
	v_add_f32_e32 v0, v14, v0
	v_mul_f32_e32 v17, v17, v17
	v_fmac_f32_e32 v16, v23, v23
	v_add_f32_e32 v0, v15, v0
	v_fmac_f32_e32 v17, v24, v24
	v_add_f32_e32 v0, v16, v0
	v_add_f32_e32 v0, v17, v0
	v_mov_b32_e32 v10, v0
	s_nop 1
	v_permlane16_swap_b32_e32 v0, v10
	v_add_f32_e32 v60, v0, v10
	v_mov_b32_e32 v61, v60
	global_load_dwordx4 v[10:13], v[38:39], off offset:2432
	global_load_dwordx4 v[14:17], v[38:39], off offset:2496
	v_permlane32_swap_b32_e32 v60, v61
	s_waitcnt vmcnt(1)
	v_lshlrev_b32_e32 v0, 16, v10
	v_and_b32_e32 v10, 0xffff0000, v10
	v_lshlrev_b32_e32 v18, 16, v11
	v_and_b32_e32 v11, 0xffff0000, v11
	v_lshlrev_b32_e32 v19, 16, v12
	v_and_b32_e32 v12, 0xffff0000, v12
	v_mul_f32_e32 v10, v10, v10
	v_mul_f32_e32 v11, v11, v11
	v_lshlrev_b32_e32 v20, 16, v13
	v_and_b32_e32 v13, 0xffff0000, v13
	v_mul_f32_e32 v12, v12, v12
	v_fmac_f32_e32 v10, v0, v0
	v_fmac_f32_e32 v11, v18, v18
	s_waitcnt vmcnt(0)
	v_lshlrev_b32_e32 v21, 16, v14
	v_and_b32_e32 v14, 0xffff0000, v14
	v_mul_f32_e32 v13, v13, v13
	v_fmac_f32_e32 v12, v19, v19
	v_add_f32_e32 v0, v10, v11
	v_lshlrev_b32_e32 v22, 16, v15
	v_and_b32_e32 v15, 0xffff0000, v15
	v_mul_f32_e32 v14, v14, v14
	v_fmac_f32_e32 v13, v20, v20
	v_add_f32_e32 v0, v12, v0
	v_lshlrev_b32_e32 v23, 16, v16
	v_and_b32_e32 v16, 0xffff0000, v16
	v_mul_f32_e32 v15, v15, v15
	v_fmac_f32_e32 v14, v21, v21
	v_add_f32_e32 v0, v13, v0
	v_lshlrev_b32_e32 v24, 16, v17
	v_and_b32_e32 v17, 0xffff0000, v17
	v_mul_f32_e32 v16, v16, v16
	v_fmac_f32_e32 v15, v22, v22
	v_add_f32_e32 v0, v14, v0
	v_mul_f32_e32 v17, v17, v17
	v_fmac_f32_e32 v16, v23, v23
	v_add_f32_e32 v0, v15, v0
	v_fmac_f32_e32 v17, v24, v24
	v_add_f32_e32 v0, v16, v0
	v_add_f32_e32 v0, v17, v0
	v_mov_b32_e32 v10, v0
	s_nop 1
	v_permlane16_swap_b32_e32 v0, v10
	v_add_f32_e32 v62, v0, v10
	v_mov_b32_e32 v63, v62
	global_load_dwordx4 v[30:33], v[38:39], off offset:2048
	global_load_dwordx4 v[26:29], v[38:39], off offset:2112
	global_load_dwordx4 v[22:25], v[38:39], off offset:2176
	global_load_dwordx4 v[18:21], v[38:39], off offset:2240
	global_load_dwordx4 v[14:17], v[38:39], off offset:2304
	global_load_dwordx4 v[10:13], v[38:39], off offset:2368
	global_load_dwordx4 v[34:37], v[38:39], off offset:2432
	s_nop 0
	global_load_dwordx4 v[38:41], v[38:39], off offset:2496
	v_xor_b32_e32 v0, v233, v42
	v_lshlrev_b32_e32 v0, 4, v0
	v_and_or_b32 v46, v0, s12, v46
	v_lshl_add_u64 v[48:49], v[46:47], 0, s[16:17]
	v_lshl_add_u64 v[64:65], s[0:1], 0, v[46:47]
	s_mov_b32 s12, m0
	s_mov_b32 m0, s93
	s_nop 0
	global_load_lds_dwordx4 v[64:65], off
	s_mov_b32 m0, s12
	v_lshl_add_u64 v[64:65], s[0:1], 0, v[48:49]
	s_add_i32 s0, s93, 0x2000
	s_mov_b32 s1, m0
	s_mov_b32 m0, s0
	s_nop 0
	global_load_lds_dwordx4 v[64:65], off
	s_mov_b32 m0, s1
	s_cmp_gt_i32 s50, 0
	v_permlane32_swap_b32_e32 v62, v63
	s_cselect_b64 s[46:47], -1, 0
	s_cmp_lt_i32 s50, 1
	v_or_b32_e32 v0, s13, v232
	s_cbranch_scc1 .LBB0_510
	s_waitcnt lgkmcnt(1)
	v_mov_b32_e32 v64, v6
	s_waitcnt lgkmcnt(0)
	v_mov_b32_e32 v65, v2
	v_mov_b32_e32 v2, v7
	v_mov_b32_e32 v6, v8
	v_mov_b32_e32 v7, v4
	v_mov_b32_e32 v4, v9
	v_pk_add_f32 v[2:3], v[64:65], v[2:3]
	v_pk_add_f32 v[4:5], v[6:7], v[4:5]
	v_lshlrev_b32_e32 v45, 16, v50
	v_pk_add_f32 v[2:3], v[2:3], v[4:5]
	v_mul_f32_e32 v66, 0x3d800000, v45
	v_add_f32_e32 v2, v2, v3
	v_mul_f32_e32 v2, 0x39000000, v2
	v_mul_f32_e32 v3, 0x4f800000, v2
	v_cmp_gt_f32_e64 s[0:1], s78, v2
	v_and_b32_e32 v45, 0xffff0000, v50
	v_mul_f32_e32 v67, 0x3d800000, v45
	v_cndmask_b32_e64 v2, v2, v3, s[0:1]
	v_sqrt_f32_e32 v3, v2
	s_mov_b32 s12, 0x40400000
	v_cmp_lt_f32_e64 s[30:31], 0, v66
	v_cmp_lt_f32_e32 vcc, 0, v67
	v_add_u32_e32 v4, -1, v3
	v_fma_f32 v5, -v4, v3, v2
	v_cmp_ge_f32_e64 s[40:41], 0, v5
	v_add_u32_e32 v5, 1, v3
	v_lshlrev_b32_e32 v45, 16, v51
	v_cndmask_b32_e64 v4, v3, v4, s[40:41]
	v_fma_f32 v3, -v5, v3, v2
	v_cmp_lt_f32_e64 s[40:41], 0, v3
	v_mul_f32_e32 v68, 0x3d800000, v45
	v_cmp_lt_f32_e64 s[34:35], 0, v68
	v_cndmask_b32_e64 v3, v4, v5, s[40:41]
	v_add_f32_e32 v5, v56, v57
	v_mul_f32_e32 v6, 0x4f800000, v5
	v_cmp_gt_f32_e64 s[40:41], s78, v5
	v_mul_f32_e32 v4, 0x37800000, v3
	v_cndmask_b32_e64 v3, v3, v4, s[0:1]
	v_cndmask_b32_e64 v5, v5, v6, s[40:41]
	v_sqrt_f32_e32 v6, v5
	v_cmp_class_f32_e64 s[0:1], v2, v231
	v_and_b32_e32 v45, 0xffff0000, v51
	v_mul_f32_e32 v69, 0x3d800000, v45
	v_cndmask_b32_e64 v2, v3, v2, s[0:1]
	v_add_u32_e32 v3, -1, v6
	v_fma_f32 v4, -v3, v6, v5
	v_cmp_ge_f32_e64 s[0:1], 0, v4
	v_add_u32_e32 v4, 1, v6
	v_cmp_lt_f32_e64 s[36:37], 0, v69
	v_cndmask_b32_e64 v3, v6, v3, s[0:1]
	v_fma_f32 v6, -v4, v6, v5
	v_cmp_lt_f32_e64 s[0:1], 0, v6
	v_mov_b32_e32 v55, 0xff800000
	v_mov_b32_e32 v70, 0x7f800000
	v_cndmask_b32_e64 v3, v3, v4, s[0:1]
	v_mul_f32_e32 v4, 0x37800000, v3
	v_cndmask_b32_e64 v3, v3, v4, s[40:41]
	v_cmp_class_f32_e64 s[0:1], v5, v231
	v_add_f32_e32 v4, v58, v59
	v_cndmask_b32_e64 v51, v55, 0, vcc
	v_cndmask_b32_e64 v3, v3, v5, s[0:1]
	v_mul_f32_e32 v5, 0x4f800000, v4
	v_cmp_gt_f32_e64 s[0:1], s78, v4
	v_mul_f32_e64 v3, |v66|, v3
	v_mul_f32_e32 v3, v2, v3
	v_cndmask_b32_e64 v4, v4, v5, s[0:1]
	v_sqrt_f32_e32 v5, v4
	v_fma_f32 v3, v3, s12, 0
	v_cndmask_b32_e64 v6, 0, v3, s[30:31]
	v_cndmask_b32_e64 v3, v3, 0, s[30:31]
	v_add_u32_e32 v7, -1, v5
	v_fma_f32 v8, -v7, v5, v4
	v_cmp_ge_f32_e64 s[40:41], 0, v8
	v_add_u32_e32 v8, 1, v5
	s_mov_b32 s12, 0x467c0400
	v_cndmask_b32_e64 v7, v5, v7, s[40:41]
	v_fma_f32 v5, -v8, v5, v4
	v_cmp_lt_f32_e64 s[40:41], 0, v5
	v_cndmask_b32_e64 v45, v55, 0, s[30:31]
	v_cndmask_b32_e64 v50, 0, v70, s[30:31]
	v_cndmask_b32_e64 v5, v7, v8, s[40:41]
	v_mul_f32_e32 v7, 0x37800000, v5
	v_cndmask_b32_e64 v5, v5, v7, s[0:1]
	v_cmp_class_f32_e64 s[0:1], v4, v231
	v_readlane_b32 s30, v251, 39
	v_cndmask_b32_e64 v53, v55, 0, s[34:35]
	v_cndmask_b32_e64 v4, v5, v4, s[0:1]
	v_add_f32_e32 v5, v60, v61
	v_mul_f32_e32 v7, 0x4f800000, v5
	v_cmp_gt_f32_e64 s[0:1], s78, v5
	v_mul_f32_e64 v4, |v67|, v4
	v_mul_f32_e32 v4, v2, v4
	v_cndmask_b32_e64 v5, v5, v7, s[0:1]
	v_sqrt_f32_e32 v7, v5
	v_fmamk_f32 v8, v4, 0x40400000, v6
	v_cndmask_b32_e32 v6, v6, v8, vcc
	v_fmamk_f32 v4, v4, 0x40400000, v3
	v_add_u32_e32 v8, -1, v7
	v_fma_f32 v9, -v8, v7, v5
	v_cmp_ge_f32_e64 s[40:41], 0, v9
	v_add_u32_e32 v9, 1, v7
	v_cndmask_b32_e32 v3, v4, v3, vcc
	v_cndmask_b32_e64 v8, v7, v8, s[40:41]
	v_fma_f32 v7, -v9, v7, v5
	v_cmp_lt_f32_e64 s[40:41], 0, v7
	v_cndmask_b32_e64 v55, v55, 0, s[36:37]
	v_cndmask_b32_e64 v57, 0, v70, s[34:35]
	v_cndmask_b32_e64 v7, v8, v9, s[40:41]
	v_mul_f32_e32 v8, 0x37800000, v7
	v_cndmask_b32_e64 v7, v7, v8, s[0:1]
	v_cmp_class_f32_e64 s[0:1], v5, v231
	v_cndmask_b32_e64 v58, 0, v70, s[36:37]
	s_mov_b32 s13, 0
	v_cndmask_b32_e64 v5, v7, v5, s[0:1]
	v_add_f32_e32 v7, v62, v63
	v_mul_f32_e32 v8, 0x4f800000, v7
	v_cmp_gt_f32_e64 s[0:1], s78, v7
	v_mul_f32_e64 v5, |v68|, v5
	v_mul_f32_e32 v5, v2, v5
	v_cndmask_b32_e64 v7, v7, v8, s[0:1]
	v_sqrt_f32_e32 v8, v7
	v_fmamk_f32 v9, v5, 0x40400000, v6
	v_cndmask_b32_e64 v6, v6, v9, s[34:35]
	v_fmamk_f32 v4, v5, 0x40400000, v3
	v_add_u32_e32 v9, -1, v8
	v_fma_f32 v56, -v9, v8, v7
	v_cmp_ge_f32_e64 s[40:41], 0, v56
	v_add_u32_e32 v56, 1, v8
	v_cndmask_b32_e64 v3, v4, v3, s[34:35]
	v_cndmask_b32_e64 v9, v8, v9, s[40:41]
	v_fma_f32 v8, -v56, v8, v7
	v_cmp_lt_f32_e64 s[40:41], 0, v8
	s_nop 1
	v_cndmask_b32_e64 v8, v9, v56, s[40:41]
	v_mul_f32_e32 v9, 0x37800000, v8
	v_cndmask_b32_e64 v8, v8, v9, s[0:1]
	v_cmp_class_f32_e64 s[0:1], v7, v231
	v_cndmask_b32_e32 v56, 0, v70, vcc
	s_waitcnt vmcnt(0)
	v_and_b32_e32 v9, 0xffff0000, v41
	v_cndmask_b32_e64 v7, v8, v7, s[0:1]
	v_mul_f32_e64 v7, |v69|, v7
	v_mul_f32_e32 v2, v2, v7
	v_fmamk_f32 v7, v2, 0x40400000, v6
	v_fmamk_f32 v2, v2, 0x40400000, v3
	v_cndmask_b32_e64 v6, v6, v7, s[36:37]
	v_cndmask_b32_e64 v2, v2, v3, s[36:37]
	v_max_f32_e32 v2, v6, v2
	v_div_scale_f32 v3, s[0:1], v2, v2, s12
	v_rcp_f32_e32 v4, v3
	v_and_b32_e32 v8, 0xffff0000, v40
	s_movk_i32 s0, 0x70
	v_readlane_b32 s1, v253, 42
	v_fma_f32 v5, -v3, v4, 1.0
	v_fmac_f32_e32 v4, v5, v4
	v_div_scale_f32 v5, vcc, s12, v2, s12
	v_mul_f32_e32 v6, v5, v4
	v_fma_f32 v7, -v3, v6, v5
	v_fmac_f32_e32 v6, v7, v4
	v_fma_f32 v3, -v3, v6, v5
	v_div_fmas_f32 v3, v3, v4, v6
	v_div_fixup_f32 v3, v3, v2, s12
	v_cmp_lt_f32_e32 vcc, 0, v2
	v_and_b32_e32 v2, 0xffff0000, v38
	v_lshlrev_b32_e32 v5, 16, v39
	v_cndmask_b32_e32 v59, 0, v3, vcc
	v_mul_f32_e32 v6, v69, v59
	v_and_b32_e32 v3, 0xffff0000, v39
	v_pk_mul_f32 v[2:3], v[6:7], v[2:3] op_sel_hi:[0,1]
	v_lshlrev_b32_e32 v4, 16, v38
	v_pk_mul_f32 v[8:9], v[6:7], v[8:9] op_sel_hi:[0,1]
	v_lshlrev_b32_e32 v39, 16, v41
	v_lshlrev_b32_e32 v38, 16, v40
	v_pk_mul_f32 v[4:5], v[6:7], v[4:5] op_sel_hi:[0,1]
	v_pk_mul_f32 v[38:39], v[6:7], v[38:39] op_sel_hi:[0,1]
	v_bfe_u32 v7, v9, 16, 1
	v_bfe_u32 v41, v3, 16, 1
	v_bfe_u32 v40, v8, 16, 1
	v_bfe_u32 v60, v2, 16, 1
	v_add3_u32 v3, v3, v41, s39
	v_add3_u32 v7, v9, v7, s39
	v_bfe_u32 v9, v4, 16, 1
	v_bfe_u32 v41, v38, 16, 1
	v_add3_u32 v2, v2, v60, s39
	v_add3_u32 v8, v8, v40, s39
	v_bfe_u32 v40, v5, 16, 1
	v_bfe_u32 v60, v39, 16, 1
	v_add3_u32 v38, v38, v41, s39
	v_add3_u32 v4, v4, v9, s39
	v_add3_u32 v39, v39, v60, s39
	v_add3_u32 v5, v5, v40, s39
	v_lshrrev_b32_e32 v9, 16, v4
	v_lshrrev_b32_e32 v4, 16, v38
	v_lshrrev_b32_e32 v40, 16, v5
	v_lshrrev_b32_e32 v5, 16, v39
	v_and_or_b32 v4, v8, s38, v4
	v_and_or_b32 v2, v2, s38, v9
	v_and_b32_e32 v9, 0xffff0000, v35
	v_and_b32_e32 v8, 0xffff0000, v34
	v_and_b32_e32 v39, 0xffff0000, v37
	v_and_b32_e32 v38, 0xffff0000, v36
	v_pk_mul_f32 v[8:9], v[6:7], v[8:9] op_sel_hi:[0,1]
	v_lshlrev_b32_e32 v35, 16, v35
	v_lshlrev_b32_e32 v34, 16, v34
	v_pk_mul_f32 v[38:39], v[6:7], v[38:39] op_sel_hi:[0,1]
	v_lshlrev_b32_e32 v37, 16, v37
	v_lshlrev_b32_e32 v36, 16, v36
	v_and_or_b32 v5, v7, s38, v5
	v_and_or_b32 v3, v3, s38, v40
	v_pk_mul_f32 v[34:35], v[6:7], v[34:35] op_sel_hi:[0,1]
	v_pk_mul_f32 v[6:7], v[6:7], v[36:37] op_sel_hi:[0,1]
	v_bfe_u32 v36, v39, 16, 1
	v_bfe_u32 v37, v38, 16, 1
	v_bfe_u32 v40, v9, 16, 1
	v_bfe_u32 v41, v8, 16, 1
	v_add3_u32 v41, v8, v41, s39
	v_add3_u32 v40, v9, v40, s39
	v_add3_u32 v8, v38, v37, s39
	v_add3_u32 v9, v39, v36, s39
	v_bfe_u32 v36, v34, 16, 1
	v_bfe_u32 v38, v6, 16, 1
	v_bfe_u32 v37, v35, 16, 1
	v_add3_u32 v6, v6, v38, s39
	v_add3_u32 v34, v34, v36, s39
	v_bfe_u32 v39, v7, 16, 1
	v_add3_u32 v35, v35, v37, s39
	v_lshrrev_b32_e32 v34, 16, v34
	v_lshrrev_b32_e32 v6, 16, v6
	v_add3_u32 v7, v7, v39, s39
	v_lshrrev_b32_e32 v35, 16, v35
	v_and_or_b32 v8, v8, s38, v6
	v_and_or_b32 v6, v41, s38, v34
	v_mul_f32_e32 v34, v68, v59
	v_and_b32_e32 v37, 0xffff0000, v11
	v_and_b32_e32 v36, 0xffff0000, v10
	v_and_b32_e32 v39, 0xffff0000, v13
	v_and_b32_e32 v38, 0xffff0000, v12
	v_lshrrev_b32_e32 v7, 16, v7
	v_pk_mul_f32 v[36:37], v[34:35], v[36:37] op_sel_hi:[0,1]
	v_lshlrev_b32_e32 v11, 16, v11
	v_lshlrev_b32_e32 v10, 16, v10
	v_pk_mul_f32 v[38:39], v[34:35], v[38:39] op_sel_hi:[0,1]
	v_lshlrev_b32_e32 v13, 16, v13
	v_lshlrev_b32_e32 v12, 16, v12
	v_and_or_b32 v9, v9, s38, v7
	v_and_or_b32 v7, v40, s38, v35
	v_pk_mul_f32 v[10:11], v[34:35], v[10:11] op_sel_hi:[0,1]
	v_pk_mul_f32 v[12:13], v[34:35], v[12:13] op_sel_hi:[0,1]
	v_bfe_u32 v35, v39, 16, 1
	v_bfe_u32 v40, v38, 16, 1
	v_bfe_u32 v41, v37, 16, 1
	v_add3_u32 v37, v37, v41, s39
	v_add3_u32 v38, v38, v40, s39
	v_add3_u32 v35, v39, v35, s39
	v_bfe_u32 v39, v10, 16, 1
	v_bfe_u32 v40, v11, 16, 1
	v_bfe_u32 v41, v12, 16, 1
	v_bfe_u32 v60, v36, 16, 1
	v_add3_u32 v12, v12, v41, s39
	v_add3_u32 v11, v11, v40, s39
	v_add3_u32 v10, v10, v39, s39
	v_add3_u32 v36, v36, v60, s39
	v_bfe_u32 v60, v13, 16, 1
	v_lshrrev_b32_e32 v10, 16, v10
	v_lshrrev_b32_e32 v11, 16, v11
	v_lshrrev_b32_e32 v12, 16, v12
	v_add3_u32 v13, v13, v60, s39
	v_and_or_b32 v12, v38, s38, v12
	v_and_or_b32 v11, v37, s38, v11
	v_and_or_b32 v10, v36, s38, v10
	v_and_b32_e32 v37, 0xffff0000, v15
	v_and_b32_e32 v36, 0xffff0000, v14
	v_and_b32_e32 v39, 0xffff0000, v17
	v_and_b32_e32 v38, 0xffff0000, v16
	v_lshrrev_b32_e32 v13, 16, v13
	v_pk_mul_f32 v[36:37], v[34:35], v[36:37] op_sel_hi:[0,1]
	v_lshlrev_b32_e32 v15, 16, v15
	v_lshlrev_b32_e32 v14, 16, v14
	v_pk_mul_f32 v[38:39], v[34:35], v[38:39] op_sel_hi:[0,1]
	v_lshlrev_b32_e32 v17, 16, v17
	v_lshlrev_b32_e32 v16, 16, v16
	v_and_or_b32 v13, v35, s38, v13
	v_pk_mul_f32 v[14:15], v[34:35], v[14:15] op_sel_hi:[0,1]
	v_pk_mul_f32 v[16:17], v[34:35], v[16:17] op_sel_hi:[0,1]
	v_bfe_u32 v34, v39, 16, 1
	v_bfe_u32 v35, v38, 16, 1
	v_bfe_u32 v41, v36, 16, 1
	v_add3_u32 v36, v36, v41, s39
	v_add3_u32 v35, v38, v35, s39
	v_add3_u32 v34, v39, v34, s39
	v_bfe_u32 v38, v14, 16, 1
	v_bfe_u32 v39, v15, 16, 1
	v_bfe_u32 v41, v17, 16, 1
	v_bfe_u32 v40, v37, 16, 1
	v_add3_u32 v17, v17, v41, s39
	v_add3_u32 v15, v15, v39, s39
	v_add3_u32 v14, v14, v38, s39
	v_add3_u32 v37, v37, v40, s39
	v_bfe_u32 v40, v16, 16, 1
	v_lshrrev_b32_e32 v14, 16, v14
	v_lshrrev_b32_e32 v15, 16, v15
	v_lshrrev_b32_e32 v17, 16, v17
	v_add3_u32 v16, v16, v40, s39
	v_and_or_b32 v17, v34, s38, v17
	v_and_or_b32 v15, v37, s38, v15
	v_and_or_b32 v14, v36, s38, v14
	v_mul_f32_e32 v34, v67, v59
	v_and_b32_e32 v37, 0xffff0000, v19
	v_and_b32_e32 v36, 0xffff0000, v18
	v_and_b32_e32 v39, 0xffff0000, v21
	v_and_b32_e32 v38, 0xffff0000, v20
	v_lshrrev_b32_e32 v16, 16, v16
	v_pk_mul_f32 v[36:37], v[34:35], v[36:37] op_sel_hi:[0,1]
	v_lshlrev_b32_e32 v19, 16, v19
	v_lshlrev_b32_e32 v18, 16, v18
	v_pk_mul_f32 v[38:39], v[34:35], v[38:39] op_sel_hi:[0,1]
	v_lshlrev_b32_e32 v21, 16, v21
	v_lshlrev_b32_e32 v20, 16, v20
	v_and_or_b32 v16, v35, s38, v16
	v_pk_mul_f32 v[18:19], v[34:35], v[18:19] op_sel_hi:[0,1]
	v_pk_mul_f32 v[20:21], v[34:35], v[20:21] op_sel_hi:[0,1]
	v_bfe_u32 v35, v39, 16, 1
	v_bfe_u32 v40, v38, 16, 1
	v_bfe_u32 v41, v37, 16, 1
	v_add3_u32 v37, v37, v41, s39
	v_add3_u32 v38, v38, v40, s39
	v_add3_u32 v35, v39, v35, s39
	v_bfe_u32 v39, v18, 16, 1
	v_bfe_u32 v40, v19, 16, 1
	v_bfe_u32 v41, v20, 16, 1
	v_bfe_u32 v60, v36, 16, 1
	v_add3_u32 v20, v20, v41, s39
	v_add3_u32 v19, v19, v40, s39
	v_add3_u32 v18, v18, v39, s39
	v_add3_u32 v36, v36, v60, s39
	v_bfe_u32 v60, v21, 16, 1
	v_lshrrev_b32_e32 v18, 16, v18
	v_lshrrev_b32_e32 v19, 16, v19
	v_lshrrev_b32_e32 v20, 16, v20
	v_add3_u32 v21, v21, v60, s39
	v_and_or_b32 v20, v38, s38, v20
	v_and_or_b32 v19, v37, s38, v19
	v_and_or_b32 v18, v36, s38, v18
	v_and_b32_e32 v37, 0xffff0000, v23
	v_and_b32_e32 v36, 0xffff0000, v22
	v_and_b32_e32 v39, 0xffff0000, v25
	v_and_b32_e32 v38, 0xffff0000, v24
	v_lshrrev_b32_e32 v21, 16, v21
	v_pk_mul_f32 v[36:37], v[34:35], v[36:37] op_sel_hi:[0,1]
	v_lshlrev_b32_e32 v23, 16, v23
	v_lshlrev_b32_e32 v22, 16, v22
	v_pk_mul_f32 v[38:39], v[34:35], v[38:39] op_sel_hi:[0,1]
	v_lshlrev_b32_e32 v25, 16, v25
	v_lshlrev_b32_e32 v24, 16, v24
	v_and_or_b32 v21, v35, s38, v21
	v_pk_mul_f32 v[22:23], v[34:35], v[22:23] op_sel_hi:[0,1]
	v_pk_mul_f32 v[24:25], v[34:35], v[24:25] op_sel_hi:[0,1]
	v_bfe_u32 v34, v39, 16, 1
	v_bfe_u32 v35, v38, 16, 1
	v_bfe_u32 v41, v36, 16, 1
	v_add3_u32 v36, v36, v41, s39
	v_add3_u32 v35, v38, v35, s39
	v_add3_u32 v34, v39, v34, s39
	v_bfe_u32 v38, v22, 16, 1
	v_bfe_u32 v39, v23, 16, 1
	v_bfe_u32 v41, v25, 16, 1
	v_bfe_u32 v40, v37, 16, 1
	v_add3_u32 v25, v25, v41, s39
	v_add3_u32 v23, v23, v39, s39
	v_add3_u32 v22, v22, v38, s39
	v_add3_u32 v37, v37, v40, s39
	v_lshrrev_b32_e32 v22, 16, v22
	v_lshrrev_b32_e32 v23, 16, v23
	v_lshrrev_b32_e32 v25, 16, v25
	v_bfe_u32 v40, v24, 16, 1
	v_and_or_b32 v25, v34, s38, v25
	v_and_or_b32 v23, v37, s38, v23
	v_and_or_b32 v22, v36, s38, v22
	v_mul_f32_e32 v34, v66, v59
	v_and_b32_e32 v37, 0xffff0000, v27
	v_and_b32_e32 v36, 0xffff0000, v26
	v_add3_u32 v24, v24, v40, s39
	v_pk_mul_f32 v[36:37], v[34:35], v[36:37] op_sel_hi:[0,1]
	v_and_b32_e32 v39, 0xffff0000, v29
	v_and_b32_e32 v38, 0xffff0000, v28
	v_lshlrev_b32_e32 v29, 16, v29
	v_lshlrev_b32_e32 v28, 16, v28
	v_lshrrev_b32_e32 v24, 16, v24
	v_lshlrev_b32_e32 v27, 16, v27
	v_lshlrev_b32_e32 v26, 16, v26
	v_pk_mul_f32 v[38:39], v[34:35], v[38:39] op_sel_hi:[0,1]
	v_pk_mul_f32 v[28:29], v[34:35], v[28:29] op_sel_hi:[0,1]
	v_bfe_u32 v41, v37, 16, 1
	v_and_or_b32 v24, v35, s38, v24
	v_pk_mul_f32 v[26:27], v[34:35], v[26:27] op_sel_hi:[0,1]
	v_bfe_u32 v35, v39, 16, 1
	v_bfe_u32 v40, v38, 16, 1
	v_add3_u32 v37, v37, v41, s39
	v_bfe_u32 v41, v28, 16, 1
	v_bfe_u32 v59, v36, 16, 1
	v_add3_u32 v38, v38, v40, s39
	v_add3_u32 v35, v39, v35, s39
	v_bfe_u32 v39, v26, 16, 1
	v_bfe_u32 v40, v27, 16, 1
	v_add3_u32 v28, v28, v41, s39
	v_add3_u32 v36, v36, v59, s39
	v_bfe_u32 v59, v29, 16, 1
	v_add3_u32 v27, v27, v40, s39
	v_add3_u32 v26, v26, v39, s39
	v_lshrrev_b32_e32 v28, 16, v28
	v_add3_u32 v29, v29, v59, s39
	v_lshrrev_b32_e32 v26, 16, v26
	v_lshrrev_b32_e32 v27, 16, v27
	v_and_or_b32 v28, v38, s38, v28
	v_and_b32_e32 v39, 0xffff0000, v33
	v_and_b32_e32 v38, 0xffff0000, v32
	v_lshrrev_b32_e32 v29, 16, v29
	v_and_or_b32 v27, v37, s38, v27
	v_and_or_b32 v26, v36, s38, v26
	v_and_b32_e32 v37, 0xffff0000, v31
	v_and_b32_e32 v36, 0xffff0000, v30
	v_lshlrev_b32_e32 v31, 16, v31
	v_lshlrev_b32_e32 v30, 16, v30
	v_pk_mul_f32 v[38:39], v[34:35], v[38:39] op_sel_hi:[0,1]
	v_lshlrev_b32_e32 v33, 16, v33
	v_lshlrev_b32_e32 v32, 16, v32
	v_and_or_b32 v29, v35, s38, v29
	v_pk_mul_f32 v[36:37], v[34:35], v[36:37] op_sel_hi:[0,1]
	v_pk_mul_f32 v[30:31], v[34:35], v[30:31] op_sel_hi:[0,1]
	v_pk_mul_f32 v[32:33], v[34:35], v[32:33] op_sel_hi:[0,1]
	v_bfe_u32 v34, v39, 16, 1
	v_bfe_u32 v35, v38, 16, 1
	v_add3_u32 v35, v38, v35, s39
	v_add3_u32 v34, v39, v34, s39
	v_bfe_u32 v38, v30, 16, 1
	v_bfe_u32 v39, v31, 16, 1
	v_add3_u32 v31, v31, v39, s39
	v_add3_u32 v30, v30, v38, s39
	v_and_b32_e32 v38, -16, v42
	v_lshlrev_b32_e32 v39, 4, v232
	v_bfe_u32 v41, v36, 16, 1
	s_add_i32 s12, s50, -1
	v_bitop3_b32 v61, v39, v38, s0 bitop3:0x6c
	v_add_u32_e32 v38, 64, v38
	v_add3_u32 v36, v36, v41, s39
	v_bfe_u32 v41, v33, 16, 1
	v_bitop3_b32 v38, v39, v38, s0 bitop3:0x6c
	s_lshl_b32 s0, s12, 5
	v_add3_u32 v33, v33, v41, s39
	v_lshlrev_b32_e32 v59, 7, v232
	v_ashrrev_i32_e32 v41, 2, v42
	s_add_i32 s0, s0, s30
	v_bfe_u32 v40, v37, 16, 1
	v_and_b32_e32 v60, -4, v41
	v_add3_u32 v41, v38, v59, s1
	v_add3_u32 v59, v61, v59, s1
	s_ashr_i32 s1, s0, 31
	v_add3_u32 v37, v37, v40, s39
	v_bfe_u32 v40, v32, 16, 1
	s_lshl_b64 s[0:1], s[0:1], 9
	v_add3_u32 v32, v32, v40, s39
	v_lshrrev_b32_e32 v30, 16, v30
	v_lshrrev_b32_e32 v31, 16, v31
	s_add_u32 s0, s4, s0
	v_lshrrev_b32_e32 v32, 16, v32
	v_lshrrev_b32_e32 v33, 16, v33
	v_and_or_b32 v31, v37, s38, v31
	v_and_or_b32 v30, v36, s38, v30
	v_lshlrev_b64 v[36:37], 3, v[42:43]
	s_addc_u32 s1, s5, s1
	v_and_or_b32 v33, v34, s38, v33
	v_and_or_b32 v32, v35, s38, v32
	v_lshl_add_u64 v[34:35], s[4:5], 0, v[36:37]
	v_lshl_add_u64 v[36:37], s[0:1], 0, v[36:37]
	s_lshl_b32 s0, s50, 7
	v_readlane_b32 s1, v254, 10
	s_add_i32 s0, s1, s0
	v_lshl_add_u32 v40, v0, 10, 0
	v_add_u32_e32 v60, s0, v60
	s_mov_b32 s0, 0
	s_waitcnt vmcnt(0)
	s_branch .LBB0_500
.LBB0_499:
	s_waitcnt vmcnt(4)
	s_add_i32 s30, s30, 32
	s_addk_i32 s13, 0x4000
	s_cmp_lg_u32 s72, s50
	s_mov_b32 s0, s72
	s_cbranch_scc0 .LBB0_510
.LBB0_500:
	s_add_i32 s72, s0, 1
	s_cmp_ge_i32 s72, s50
	s_barrier
	s_cbranch_scc1 .LBB0_502
	s_lshl_b64 s[34:35], s[72:73], 16
	s_add_u32 s1, s42, s34
	s_addc_u32 s31, s43, s35
	s_add_u32 s34, s1, 0x100
	s_addc_u32 s35, s31, 0
	s_lshl_b32 s1, s72, 14
	s_and_b32 s1, s1, 0x4000
	v_lshl_add_u64 v[38:39], s[34:35], 0, v[46:47]
	s_add_i32 s1, s1, s93
	s_mov_b32 s31, m0
	s_mov_b32 m0, s1
	s_nop 0
	global_load_lds_dwordx4 v[38:39], off
	s_mov_b32 m0, s31
	v_lshl_add_u64 v[38:39], s[34:35], 0, v[48:49]
	s_addk_i32 s1, 0x2000
	s_mov_b32 s31, m0
	s_mov_b32 m0, s1
	s_nop 0
	global_load_lds_dwordx4 v[38:39], off
	s_mov_b32 m0, s31

.LBB0_789:
	s_and_b32 s1, s13, 0x4000
	v_add_u32_e32 v61, s1, v41
	v_add_u32_e32 v62, s1, v59
	s_cmp_eq_u32 s0, s12
	s_mov_b64 s[0:1], -1
	s_cbranch_scc1 .LBB0_793
	s_mov_b32 s0, s30
	s_ashr_i32 s1, s0, 31
	s_lshl_b64 s[34:35], s[0:1], 9
	ds_read_b128 v[72:75], v62
	ds_read_b128 v[76:79], v61
	ds_read_b128 v[80:83], v62 offset:4096
	ds_read_b128 v[84:87], v61 offset:4096
	ds_read_b128 v[88:91], v62 offset:8192
	ds_read_b128 v[92:95], v61 offset:8192
	ds_read_b128 v[96:99], v62 offset:12288
	ds_read_b128 v[100:103], v61 offset:12288
	v_lshl_add_u64 v[168:169], v[34:35], 0, s[34:35]
	s_waitcnt lgkmcnt(7)
	v_mfma_f32_16x16x32_bf16 v[104:107], v[72:75], v[30:33], 0
	v_mfma_f32_16x16x32_bf16 v[108:111], v[72:75], v[22:25], 0
	v_mfma_f32_16x16x32_bf16 v[112:115], v[72:75], v[14:17], 0
	v_mfma_f32_16x16x32_bf16 v[116:119], v[72:75], v[6:9], 0
	s_waitcnt lgkmcnt(6)
	v_mfma_f32_16x16x32_bf16 v[104:107], v[76:79], v[26:29], v[104:107]
	v_mfma_f32_16x16x32_bf16 v[108:111], v[76:79], v[18:21], v[108:111]
	v_mfma_f32_16x16x32_bf16 v[112:115], v[76:79], v[10:13], v[112:115]
	v_mfma_f32_16x16x32_bf16 v[116:119], v[76:79], v[2:5], v[116:119]
	s_waitcnt lgkmcnt(5)
	v_mfma_f32_16x16x32_bf16 v[120:123], v[80:83], v[30:33], 0
	v_mfma_f32_16x16x32_bf16 v[124:127], v[80:83], v[22:25], 0
	v_mfma_f32_16x16x32_bf16 v[128:131], v[80:83], v[14:17], 0
	v_mfma_f32_16x16x32_bf16 v[132:135], v[80:83], v[6:9], 0
	s_waitcnt lgkmcnt(4)
	v_mfma_f32_16x16x32_bf16 v[120:123], v[84:87], v[26:29], v[120:123]
	v_mfma_f32_16x16x32_bf16 v[124:127], v[84:87], v[18:21], v[124:127]
	v_mfma_f32_16x16x32_bf16 v[128:131], v[84:87], v[10:13], v[128:131]
	v_mfma_f32_16x16x32_bf16 v[132:135], v[84:87], v[2:5], v[132:135]
	s_waitcnt lgkmcnt(0)
	v_med3_f32 v170, v104, v45, v50
	v_med3_f32 v178, v108, v51, v56
	v_med3_f32 v171, v112, v53, v57
	v_med3_f32 v179, v116, v55, v58
	v_med3_f32 v172, v105, v45, v50
	v_med3_f32 v180, v109, v51, v56
	v_mfma_f32_16x16x32_bf16 v[136:139], v[88:91], v[30:33], 0
	v_med3_f32 v173, v113, v53, v57
	v_med3_f32 v181, v117, v55, v58
	v_med3_f32 v174, v106, v45, v50
	v_med3_f32 v182, v110, v51, v56
	v_med3_f32 v175, v114, v53, v57
	v_med3_f32 v183, v118, v55, v58
	v_mfma_f32_16x16x32_bf16 v[140:143], v[88:91], v[22:25], 0
	v_med3_f32 v176, v107, v45, v50
	v_med3_f32 v184, v111, v51, v56
	v_med3_f32 v177, v115, v53, v57
	v_med3_f32 v185, v119, v55, v58
	v_pk_add_f32 v[170:171], v[170:171], v[178:179]
	v_pk_add_f32 v[172:173], v[172:173], v[180:181]
	v_mfma_f32_16x16x32_bf16 v[144:147], v[88:91], v[14:17], 0
	v_pk_add_f32 v[174:175], v[174:175], v[182:183]
	v_pk_add_f32 v[176:177], v[176:177], v[184:185]
	v_add_f32_e32 v186, v170, v171
	v_add_f32_e32 v187, v172, v173
	v_add_f32_e32 v188, v174, v175
	v_add_f32_e32 v189, v176, v177
	v_mfma_f32_16x16x32_bf16 v[148:151], v[88:91], v[6:9], 0
	v_cvt_pkrtz_f16_f32 v190, v186, v187
	v_cvt_pkrtz_f16_f32 v191, v188, v189
	global_store_dwordx2 v[168:169], v[190:191], off
	v_cvt_f32_f16_e32 v192, v190
	v_cvt_f32_f16_sdwa v193, v190 dst_sel:DWORD dst_unused:UNUSED_PAD src0_sel:WORD_1
	v_cvt_f32_f16_e32 v194, v191
	v_mfma_f32_16x16x32_bf16 v[136:139], v[92:95], v[26:29], v[136:139]
	v_cvt_f32_f16_sdwa v195, v191 dst_sel:DWORD dst_unused:UNUSED_PAD src0_sel:WORD_1
	v_sqrt_f32_e64 v170, |v192|
	v_sqrt_f32_e64 v171, |v193|
	v_sqrt_f32_e64 v172, |v194|
	v_sqrt_f32_e64 v173, |v195|
	v_ceil_f32_e32 v170, v170
	v_mfma_f32_16x16x32_bf16 v[140:143], v[92:95], v[18:21], v[140:143]
	v_ceil_f32_e32 v171, v171
	v_ceil_f32_e32 v172, v172
	v_ceil_f32_e32 v173, v173
	v_min_f32_e32 v170, 0x42fe0000, v170
	v_min_f32_e32 v171, 0x42fe0000, v171
	v_min_f32_e32 v172, 0x42fe0000, v172
	v_mfma_f32_16x16x32_bf16 v[144:147], v[92:95], v[10:13], v[144:147]
	v_min_f32_e32 v173, 0x42fe0000, v173
	v_bfi_b32 v170, s10, v170, v192
	v_bfi_b32 v171, s10, v171, v193
	v_bfi_b32 v172, s10, v172, v194
	v_bfi_b32 v173, s10, v173, v195
	v_cvt_i32_f32_e32 v170, v170
	v_mfma_f32_16x16x32_bf16 v[148:151], v[92:95], v[2:5], v[148:151]
	v_cvt_i32_f32_e32 v171, v171
	v_cvt_i32_f32_e32 v172, v172
	v_cvt_i32_f32_e32 v173, v173
	v_lshl_add_u32 v170, v170, 2, v40
	v_lshl_add_u32 v171, v171, 2, v40
	v_lshl_add_u32 v172, v172, 2, v40
	v_lshl_add_u32 v173, v173, 2, v40
	ds_add_u32 v170, v245 offset:33280
	ds_add_u32 v171, v245 offset:33280
	ds_add_u32 v172, v245 offset:33280
	ds_add_u32 v173, v245 offset:33280
	v_med3_f32 v170, v120, v45, v50
	v_med3_f32 v178, v124, v51, v56
	v_med3_f32 v171, v128, v53, v57
	v_med3_f32 v179, v132, v55, v58
	v_med3_f32 v172, v121, v45, v50
	v_med3_f32 v180, v125, v51, v56
	v_mfma_f32_16x16x32_bf16 v[152:155], v[96:99], v[30:33], 0
	v_med3_f32 v173, v129, v53, v57
	v_med3_f32 v181, v133, v55, v58
	v_med3_f32 v174, v122, v45, v50
	v_med3_f32 v182, v126, v51, v56
	v_med3_f32 v175, v130, v53, v57
	v_med3_f32 v183, v134, v55, v58
	v_mfma_f32_16x16x32_bf16 v[156:159], v[96:99], v[22:25], 0
	v_med3_f32 v176, v123, v45, v50
	v_med3_f32 v184, v127, v51, v56
	v_med3_f32 v177, v131, v53, v57
	v_med3_f32 v185, v135, v55, v58
	v_pk_add_f32 v[170:171], v[170:171], v[178:179]
	v_pk_add_f32 v[172:173], v[172:173], v[180:181]
	v_mfma_f32_16x16x32_bf16 v[160:163], v[96:99], v[14:17], 0
	v_pk_add_f32 v[174:175], v[174:175], v[182:183]
	v_pk_add_f32 v[176:177], v[176:177], v[184:185]
	v_add_f32_e32 v186, v170, v171
	v_add_f32_e32 v187, v172, v173
	v_add_f32_e32 v188, v174, v175
	v_add_f32_e32 v189, v176, v177
	v_mfma_f32_16x16x32_bf16 v[164:167], v[96:99], v[6:9], 0
	v_cvt_pkrtz_f16_f32 v190, v186, v187
	v_cvt_pkrtz_f16_f32 v191, v188, v189
	global_store_dwordx2 v[168:169], v[190:191], off offset:512
	v_cvt_f32_f16_e32 v192, v190
	v_cvt_f32_f16_sdwa v193, v190 dst_sel:DWORD dst_unused:UNUSED_PAD src0_sel:WORD_1
	v_cvt_f32_f16_e32 v194, v191
	v_mfma_f32_16x16x32_bf16 v[152:155], v[100:103], v[26:29], v[152:155]
	v_cvt_f32_f16_sdwa v195, v191 dst_sel:DWORD dst_unused:UNUSED_PAD src0_sel:WORD_1
	v_sqrt_f32_e64 v170, |v192|
	v_sqrt_f32_e64 v171, |v193|
	v_sqrt_f32_e64 v172, |v194|
	v_sqrt_f32_e64 v173, |v195|
	v_ceil_f32_e32 v170, v170
	v_mfma_f32_16x16x32_bf16 v[156:159], v[100:103], v[18:21], v[156:159]
	v_ceil_f32_e32 v171, v171
	v_ceil_f32_e32 v172, v172
	v_ceil_f32_e32 v173, v173
	v_min_f32_e32 v170, 0x42fe0000, v170
	v_min_f32_e32 v171, 0x42fe0000, v171
	v_min_f32_e32 v172, 0x42fe0000, v172
	v_mfma_f32_16x16x32_bf16 v[160:163], v[100:103], v[10:13], v[160:163]
	v_min_f32_e32 v173, 0x42fe0000, v173
	v_bfi_b32 v170, s10, v170, v192
	v_bfi_b32 v171, s10, v171, v193
	v_bfi_b32 v172, s10, v172, v194
	v_bfi_b32 v173, s10, v173, v195
	v_cvt_i32_f32_e32 v170, v170
	v_mfma_f32_16x16x32_bf16 v[164:167], v[100:103], v[2:5], v[164:167]
	v_cvt_i32_f32_e32 v171, v171
	v_cvt_i32_f32_e32 v172, v172
	v_cvt_i32_f32_e32 v173, v173
	v_lshl_add_u32 v170, v170, 2, v40
	v_lshl_add_u32 v171, v171, 2, v40
	v_lshl_add_u32 v172, v172, 2, v40
	v_lshl_add_u32 v173, v173, 2, v40
	ds_add_u32 v170, v245 offset:33280
	ds_add_u32 v171, v245 offset:33280
	ds_add_u32 v172, v245 offset:33280
	ds_add_u32 v173, v245 offset:33280
	v_med3_f32 v170, v136, v45, v50
	v_med3_f32 v178, v140, v51, v56
	v_med3_f32 v171, v144, v53, v57
	v_med3_f32 v179, v148, v55, v58
	v_med3_f32 v172, v137, v45, v50
	v_med3_f32 v180, v141, v51, v56
	v_med3_f32 v173, v145, v53, v57
	v_med3_f32 v181, v149, v55, v58
	v_med3_f32 v174, v138, v45, v50
	v_med3_f32 v182, v142, v51, v56
	v_med3_f32 v175, v146, v53, v57
	v_med3_f32 v183, v150, v55, v58
	v_med3_f32 v176, v139, v45, v50
	v_med3_f32 v184, v143, v51, v56
	v_med3_f32 v177, v147, v53, v57
	v_med3_f32 v185, v151, v55, v58
	v_pk_add_f32 v[170:171], v[170:171], v[178:179]
	v_pk_add_f32 v[172:173], v[172:173], v[180:181]
	v_pk_add_f32 v[174:175], v[174:175], v[182:183]
	v_pk_add_f32 v[176:177], v[176:177], v[184:185]
	v_add_f32_e32 v186, v170, v171
	v_add_f32_e32 v187, v172, v173
	v_add_f32_e32 v188, v174, v175
	v_add_f32_e32 v189, v176, v177
	v_cvt_pkrtz_f16_f32 v190, v186, v187
	v_cvt_pkrtz_f16_f32 v191, v188, v189
	global_store_dwordx2 v[168:169], v[190:191], off offset:1024
	v_cvt_f32_f16_e32 v192, v190
	v_cvt_f32_f16_sdwa v193, v190 dst_sel:DWORD dst_unused:UNUSED_PAD src0_sel:WORD_1
	v_cvt_f32_f16_e32 v194, v191
	v_cvt_f32_f16_sdwa v195, v191 dst_sel:DWORD dst_unused:UNUSED_PAD src0_sel:WORD_1
	v_sqrt_f32_e64 v170, |v192|
	v_sqrt_f32_e64 v171, |v193|
	v_sqrt_f32_e64 v172, |v194|
	v_sqrt_f32_e64 v173, |v195|
	v_ceil_f32_e32 v170, v170
	v_ceil_f32_e32 v171, v171
	v_ceil_f32_e32 v172, v172
	v_ceil_f32_e32 v173, v173
	v_min_f32_e32 v170, 0x42fe0000, v170
	v_min_f32_e32 v171, 0x42fe0000, v171
	v_min_f32_e32 v172, 0x42fe0000, v172
	v_min_f32_e32 v173, 0x42fe0000, v173
	v_bfi_b32 v170, s10, v170, v192
	v_bfi_b32 v171, s10, v171, v193
	v_bfi_b32 v172, s10, v172, v194
	v_bfi_b32 v173, s10, v173, v195
	v_cvt_i32_f32_e32 v170, v170
	v_cvt_i32_f32_e32 v171, v171
	v_cvt_i32_f32_e32 v172, v172
	v_cvt_i32_f32_e32 v173, v173
	v_lshl_add_u32 v170, v170, 2, v40
	v_lshl_add_u32 v171, v171, 2, v40
	v_lshl_add_u32 v172, v172, 2, v40
	v_lshl_add_u32 v173, v173, 2, v40
	ds_add_u32 v170, v245 offset:33280
	ds_add_u32 v171, v245 offset:33280
	ds_add_u32 v172, v245 offset:33280
	ds_add_u32 v173, v245 offset:33280
	v_med3_f32 v170, v152, v45, v50
	v_med3_f32 v178, v156, v51, v56
	v_med3_f32 v171, v160, v53, v57
	v_med3_f32 v179, v164, v55, v58
	v_med3_f32 v172, v153, v45, v50
	v_med3_f32 v180, v157, v51, v56
	v_med3_f32 v173, v161, v53, v57
	v_med3_f32 v181, v165, v55, v58
	v_med3_f32 v174, v154, v45, v50
	v_med3_f32 v182, v158, v51, v56
	v_med3_f32 v175, v162, v53, v57
	v_med3_f32 v183, v166, v55, v58
	v_med3_f32 v176, v155, v45, v50
	v_med3_f32 v184, v159, v51, v56
	v_med3_f32 v177, v163, v53, v57
	v_med3_f32 v185, v167, v55, v58
	v_pk_add_f32 v[170:171], v[170:171], v[178:179]
	v_pk_add_f32 v[172:173], v[172:173], v[180:181]
	v_pk_add_f32 v[174:175], v[174:175], v[182:183]
	v_pk_add_f32 v[176:177], v[176:177], v[184:185]
	v_add_f32_e32 v186, v170, v171
	v_add_f32_e32 v187, v172, v173
	v_add_f32_e32 v188, v174, v175
	v_add_f32_e32 v189, v176, v177
	v_cvt_pkrtz_f16_f32 v190, v186, v187
	v_cvt_pkrtz_f16_f32 v191, v188, v189
	global_store_dwordx2 v[168:169], v[190:191], off offset:1536
	v_cvt_f32_f16_e32 v192, v190
	v_cvt_f32_f16_sdwa v193, v190 dst_sel:DWORD dst_unused:UNUSED_PAD src0_sel:WORD_1
	v_cvt_f32_f16_e32 v194, v191
	v_cvt_f32_f16_sdwa v195, v191 dst_sel:DWORD dst_unused:UNUSED_PAD src0_sel:WORD_1
	v_sqrt_f32_e64 v170, |v192|
	v_sqrt_f32_e64 v171, |v193|
	v_sqrt_f32_e64 v172, |v194|
	v_sqrt_f32_e64 v173, |v195|
	v_ceil_f32_e32 v170, v170
	v_ceil_f32_e32 v171, v171
	v_ceil_f32_e32 v172, v172
	v_ceil_f32_e32 v173, v173
	v_min_f32_e32 v170, 0x42fe0000, v170
	v_min_f32_e32 v171, 0x42fe0000, v171
	v_min_f32_e32 v172, 0x42fe0000, v172
	v_min_f32_e32 v173, 0x42fe0000, v173
	v_bfi_b32 v170, s10, v170, v192
	v_bfi_b32 v171, s10, v171, v193
	v_bfi_b32 v172, s10, v172, v194
	v_bfi_b32 v173, s10, v173, v195
	v_cvt_i32_f32_e32 v170, v170
	v_cvt_i32_f32_e32 v171, v171
	v_cvt_i32_f32_e32 v172, v172
	v_cvt_i32_f32_e32 v173, v173
	v_lshl_add_u32 v170, v170, 2, v40
	v_lshl_add_u32 v171, v171, 2, v40
	v_lshl_add_u32 v172, v172, 2, v40
	v_lshl_add_u32 v173, v173, 2, v40
	ds_add_u32 v170, v245 offset:33280
	ds_add_u32 v171, v245 offset:33280
	ds_add_u32 v172, v245 offset:33280
	ds_add_u32 v173, v245 offset:33280
	s_mov_b64 s[0:1], 0

.LBB0_1381:
	v_mov_b32_e32 v34, v1
	s_lshl_b32 s17, s56, 8
	v_mbcnt_lo_u32_b32 v34, -1, v34
	v_mbcnt_hi_u32_b32 v34, -1, v34
	s_add_i32 s15, s17, s51
	v_readlane_b32 s19, v253, 24
	v_and_or_b32 v185, v34, 15, s15
	s_sub_i32 s34, s56, s19
	v_ashrrev_i32_e32 v34, 1, v34
	v_subrev_u32_e32 v156, s17, v185
	s_lshl_b32 s17, s34, 7
	v_and_b32_e32 v34, -8, v34
	s_lshl_b32 s15, s64, 10
	s_and_b32 s17, s17, 0xfffffc00
	v_add_u32_e32 v34, s52, v34
	v_lshl_add_u32 v152, s57, 7, v34
	v_lshl_add_u32 v34, v34, 2, s15
	v_lshl_add_u32 v156, v156, 2, s17
	v_add_u32_e32 v138, 0x20800, v34
	v_add_u32_e32 v157, 0x20000, v156
	ds_read_b128 v[160:163], v138
	ds_read_b128 v[164:167], v138 offset:16
	ds_read_b128 v[168:171], v138 offset:512
	ds_read_b128 v[172:175], v138 offset:528
	ds_read2_b32 v[176:177], v157 offset1:16
	ds_read2_b32 v[178:179], v157 offset0:32 offset1:48
	ds_read2_b32 v[180:181], v157 offset0:128 offset1:144
	ds_read2_b32 v[182:183], v157 offset0:160 offset1:176
	s_movk_i32 s17, 0xb00
	s_ashr_i32 s15, s56, 4
	s_mul_i32 s15, s15, 0x700000
	s_mov_b32 s100, 0xbfb8aa3b
	s_mov_b32 s101, 0xbfb8aa3b
	v_mad_u32_u24 v184, v185, s17, v152
	v_mov_b32_e32 v186, 1.0
	v_mov_b32_e32 v187, 1.0
	v_add_u32_e32 v184, s15, v184
	v_cvt_f32_i32_e32 v134, v134
	v_cvt_f32_i32_e32 v135, v135
	v_cvt_f32_i32_e32 v136, v136
	v_cvt_f32_i32_e32 v137, v137
	v_cvt_f32_i32_e32 v126, v126
	v_cvt_f32_i32_e32 v127, v127
	v_cvt_f32_i32_e32 v128, v128
	v_cvt_f32_i32_e32 v129, v129
	v_cvt_f32_i32_e32 v130, v130
	v_cvt_f32_i32_e32 v131, v131
	v_cvt_f32_i32_e32 v132, v132
	v_cvt_f32_i32_e32 v133, v133
	v_cvt_f32_i32_e32 v122, v122
	v_cvt_f32_i32_e32 v123, v123
	v_cvt_f32_i32_e32 v124, v124
	v_cvt_f32_i32_e32 v125, v125
	s_waitcnt lgkmcnt(0)
	v_mul_f32_e32 v168, 0x41000000, v168
	v_mul_f32_e32 v169, 0x41000000, v169
	v_mul_f32_e32 v170, 0x41000000, v170
	v_mul_f32_e32 v171, 0x41000000, v171
	v_mul_f32_e32 v172, 0x41000000, v172
	v_mul_f32_e32 v173, 0x41000000, v173
	v_mul_f32_e32 v174, 0x41000000, v174
	v_mul_f32_e32 v175, 0x41000000, v175
	v_pk_mul_f32 v[188:189], v[160:161], v[176:177] op_sel_hi:[1,0]
	v_pk_mul_f32 v[190:191], v[162:163], v[176:177] op_sel_hi:[1,0]
	v_pk_mul_f32 v[192:193], v[164:165], v[176:177] op_sel_hi:[1,0]
	v_pk_mul_f32 v[194:195], v[166:167], v[176:177] op_sel_hi:[1,0]
	v_pk_mul_f32 v[196:197], v[168:169], v[176:177] op_sel_hi:[1,0]
	v_pk_mul_f32 v[198:199], v[170:171], v[176:177] op_sel_hi:[1,0]
	v_pk_mul_f32 v[204:205], v[172:173], v[176:177] op_sel_hi:[1,0]
	v_pk_mul_f32 v[206:207], v[174:175], v[176:177] op_sel_hi:[1,0]
	v_pk_mul_f32 v[134:135], v[188:189], v[134:135]
	v_pk_mul_f32 v[136:137], v[190:191], v[136:137]
	v_pk_mul_f32 v[126:127], v[192:193], v[126:127]
	v_pk_mul_f32 v[128:129], v[194:195], v[128:129]
	v_pk_mul_f32 v[130:131], v[196:197], v[130:131]
	v_pk_mul_f32 v[132:133], v[198:199], v[132:133]
	v_pk_mul_f32 v[122:123], v[204:205], v[122:123]
	v_pk_mul_f32 v[124:125], v[206:207], v[124:125]
	v_pk_mul_f32 v[208:209], v[134:135], s[100:101]
	v_pk_mul_f32 v[210:211], v[136:137], s[100:101]
	v_pk_mul_f32 v[212:213], v[126:127], s[100:101]
	v_pk_mul_f32 v[214:215], v[128:129], s[100:101]
	v_exp_f32_e32 v208, v208
	v_exp_f32_e32 v209, v209
	v_exp_f32_e32 v210, v210
	v_exp_f32_e32 v211, v211
	v_exp_f32_e32 v212, v212
	v_exp_f32_e32 v213, v213
	v_exp_f32_e32 v214, v214
	v_exp_f32_e32 v215, v215
	v_pk_add_f32 v[208:209], v[208:209], v[186:187]
	v_pk_add_f32 v[210:211], v[210:211], v[186:187]
	v_pk_add_f32 v[212:213], v[212:213], v[186:187]
	v_pk_add_f32 v[214:215], v[214:215], v[186:187]
	v_rcp_f32_e32 v208, v208
	v_rcp_f32_e32 v209, v209
	v_rcp_f32_e32 v210, v210
	v_rcp_f32_e32 v211, v211
	v_rcp_f32_e32 v212, v212
	v_rcp_f32_e32 v213, v213
	v_rcp_f32_e32 v214, v214
	v_rcp_f32_e32 v215, v215
	v_pk_mul_f32 v[208:209], v[134:135], v[208:209]
	v_pk_mul_f32 v[210:211], v[136:137], v[210:211]
	v_pk_mul_f32 v[212:213], v[126:127], v[212:213]
	v_pk_mul_f32 v[214:215], v[128:129], v[214:215]
	v_pk_mul_f32 v[208:209], v[130:131], v[208:209]
	v_pk_mul_f32 v[210:211], v[132:133], v[210:211]
	v_pk_mul_f32 v[212:213], v[122:123], v[212:213]
	v_pk_mul_f32 v[214:215], v[124:125], v[214:215]
	v_med3_f32 v208, v208, s97, v230
	v_med3_f32 v209, v209, s97, v230
	v_med3_f32 v210, v210, s97, v230
	v_med3_f32 v211, v211, s97, v230
	v_med3_f32 v212, v212, s97, v230
	v_med3_f32 v213, v213, s97, v230
	v_med3_f32 v214, v214, s97, v230
	v_med3_f32 v215, v215, s97, v230
	v_cvt_pk_fp8_f32 v134, v208, v209
	v_cvt_pk_fp8_f32 v135, v212, v213
	v_cvt_pk_fp8_f32 v134, v210, v211 op_sel:[0,0,1]
	v_cvt_pk_fp8_f32 v135, v214, v215 op_sel:[0,0,1]
	v_mov_b32_e32 v216, v184
	global_store_dwordx2 v216, v[134:135], s[4:5]
	v_cvt_f32_i32_e32 v118, v118
	v_cvt_f32_i32_e32 v119, v119
	v_cvt_f32_i32_e32 v120, v120
	v_cvt_f32_i32_e32 v121, v121
	v_cvt_f32_i32_e32 v110, v110
	v_cvt_f32_i32_e32 v111, v111
	v_cvt_f32_i32_e32 v112, v112
	v_cvt_f32_i32_e32 v113, v113
	v_cvt_f32_i32_e32 v114, v114
	v_cvt_f32_i32_e32 v115, v115
	v_cvt_f32_i32_e32 v116, v116
	v_cvt_f32_i32_e32 v117, v117
	v_cvt_f32_i32_e32 v106, v106
	v_cvt_f32_i32_e32 v107, v107
	v_cvt_f32_i32_e32 v108, v108
	v_cvt_f32_i32_e32 v109, v109
	v_pk_mul_f32 v[188:189], v[160:161], v[176:177] op_sel:[0,1]
	v_pk_mul_f32 v[190:191], v[162:163], v[176:177] op_sel:[0,1]
	v_pk_mul_f32 v[192:193], v[164:165], v[176:177] op_sel:[0,1]
	v_pk_mul_f32 v[194:195], v[166:167], v[176:177] op_sel:[0,1]
	v_pk_mul_f32 v[196:197], v[168:169], v[176:177] op_sel:[0,1]
	v_pk_mul_f32 v[198:199], v[170:171], v[176:177] op_sel:[0,1]
	v_pk_mul_f32 v[204:205], v[172:173], v[176:177] op_sel:[0,1]
	v_pk_mul_f32 v[206:207], v[174:175], v[176:177] op_sel:[0,1]
	v_pk_mul_f32 v[118:119], v[188:189], v[118:119]
	v_pk_mul_f32 v[120:121], v[190:191], v[120:121]
	v_pk_mul_f32 v[110:111], v[192:193], v[110:111]
	v_pk_mul_f32 v[112:113], v[194:195], v[112:113]
	v_pk_mul_f32 v[114:115], v[196:197], v[114:115]
	v_pk_mul_f32 v[116:117], v[198:199], v[116:117]
	v_pk_mul_f32 v[106:107], v[204:205], v[106:107]
	v_pk_mul_f32 v[108:109], v[206:207], v[108:109]
	v_pk_mul_f32 v[208:209], v[118:119], s[100:101]
	v_pk_mul_f32 v[210:211], v[120:121], s[100:101]
	v_pk_mul_f32 v[212:213], v[110:111], s[100:101]
	v_pk_mul_f32 v[214:215], v[112:113], s[100:101]
	v_exp_f32_e32 v208, v208
	v_exp_f32_e32 v209, v209
	v_exp_f32_e32 v210, v210
	v_exp_f32_e32 v211, v211
	v_exp_f32_e32 v212, v212
	v_exp_f32_e32 v213, v213
	v_exp_f32_e32 v214, v214
	v_exp_f32_e32 v215, v215
	v_pk_add_f32 v[208:209], v[208:209], v[186:187]
	v_pk_add_f32 v[210:211], v[210:211], v[186:187]
	v_pk_add_f32 v[212:213], v[212:213], v[186:187]
	v_pk_add_f32 v[214:215], v[214:215], v[186:187]
	v_rcp_f32_e32 v208, v208
	v_rcp_f32_e32 v209, v209
	v_rcp_f32_e32 v210, v210
	v_rcp_f32_e32 v211, v211
	v_rcp_f32_e32 v212, v212
	v_rcp_f32_e32 v213, v213
	v_rcp_f32_e32 v214, v214
	v_rcp_f32_e32 v215, v215
	v_pk_mul_f32 v[208:209], v[118:119], v[208:209]
	v_pk_mul_f32 v[210:211], v[120:121], v[210:211]
	v_pk_mul_f32 v[212:213], v[110:111], v[212:213]
	v_pk_mul_f32 v[214:215], v[112:113], v[214:215]
	v_pk_mul_f32 v[208:209], v[114:115], v[208:209]
	v_pk_mul_f32 v[210:211], v[116:117], v[210:211]
	v_pk_mul_f32 v[212:213], v[106:107], v[212:213]
	v_pk_mul_f32 v[214:215], v[108:109], v[214:215]
	v_med3_f32 v208, v208, s97, v230
	v_med3_f32 v209, v209, s97, v230
	v_med3_f32 v210, v210, s97, v230
	v_med3_f32 v211, v211, s97, v230
	v_med3_f32 v212, v212, s97, v230
	v_med3_f32 v213, v213, s97, v230
	v_med3_f32 v214, v214, s97, v230
	v_med3_f32 v215, v215, s97, v230
	v_cvt_pk_fp8_f32 v118, v208, v209
	v_cvt_pk_fp8_f32 v119, v212, v213
	v_cvt_pk_fp8_f32 v118, v210, v211 op_sel:[0,0,1]
	v_cvt_pk_fp8_f32 v119, v214, v215 op_sel:[0,0,1]
	v_add_u32_e32 v216, 0xb000, v184
	global_store_dwordx2 v216, v[118:119], s[4:5]
	v_cvt_f32_i32_e32 v102, v102
	v_cvt_f32_i32_e32 v103, v103
	v_cvt_f32_i32_e32 v104, v104
	v_cvt_f32_i32_e32 v105, v105
	v_cvt_f32_i32_e32 v94, v94
	v_cvt_f32_i32_e32 v95, v95
	v_cvt_f32_i32_e32 v96, v96
	v_cvt_f32_i32_e32 v97, v97
	v_cvt_f32_i32_e32 v98, v98
	v_cvt_f32_i32_e32 v99, v99
	v_cvt_f32_i32_e32 v100, v100
	v_cvt_f32_i32_e32 v101, v101
	v_cvt_f32_i32_e32 v90, v90
	v_cvt_f32_i32_e32 v91, v91
	v_cvt_f32_i32_e32 v92, v92
	v_cvt_f32_i32_e32 v93, v93
	v_pk_mul_f32 v[188:189], v[160:161], v[178:179] op_sel_hi:[1,0]
	v_pk_mul_f32 v[190:191], v[162:163], v[178:179] op_sel_hi:[1,0]
	v_pk_mul_f32 v[192:193], v[164:165], v[178:179] op_sel_hi:[1,0]
	v_pk_mul_f32 v[194:195], v[166:167], v[178:179] op_sel_hi:[1,0]
	v_pk_mul_f32 v[196:197], v[168:169], v[178:179] op_sel_hi:[1,0]
	v_pk_mul_f32 v[198:199], v[170:171], v[178:179] op_sel_hi:[1,0]
	v_pk_mul_f32 v[204:205], v[172:173], v[178:179] op_sel_hi:[1,0]
	v_pk_mul_f32 v[206:207], v[174:175], v[178:179] op_sel_hi:[1,0]
	v_pk_mul_f32 v[102:103], v[188:189], v[102:103]
	v_pk_mul_f32 v[104:105], v[190:191], v[104:105]
	v_pk_mul_f32 v[94:95], v[192:193], v[94:95]
	v_pk_mul_f32 v[96:97], v[194:195], v[96:97]
	v_pk_mul_f32 v[98:99], v[196:197], v[98:99]
	v_pk_mul_f32 v[100:101], v[198:199], v[100:101]
	v_pk_mul_f32 v[90:91], v[204:205], v[90:91]
	v_pk_mul_f32 v[92:93], v[206:207], v[92:93]
	v_pk_mul_f32 v[208:209], v[102:103], s[100:101]
	v_pk_mul_f32 v[210:211], v[104:105], s[100:101]
	v_pk_mul_f32 v[212:213], v[94:95], s[100:101]
	v_pk_mul_f32 v[214:215], v[96:97], s[100:101]
	v_exp_f32_e32 v208, v208
	v_exp_f32_e32 v209, v209
	v_exp_f32_e32 v210, v210
	v_exp_f32_e32 v211, v211
	v_exp_f32_e32 v212, v212
	v_exp_f32_e32 v213, v213
	v_exp_f32_e32 v214, v214
	v_exp_f32_e32 v215, v215
	v_pk_add_f32 v[208:209], v[208:209], v[186:187]
	v_pk_add_f32 v[210:211], v[210:211], v[186:187]
	v_pk_add_f32 v[212:213], v[212:213], v[186:187]
	v_pk_add_f32 v[214:215], v[214:215], v[186:187]
	v_rcp_f32_e32 v208, v208
	v_rcp_f32_e32 v209, v209
	v_rcp_f32_e32 v210, v210
	v_rcp_f32_e32 v211, v211
	v_rcp_f32_e32 v212, v212
	v_rcp_f32_e32 v213, v213
	v_rcp_f32_e32 v214, v214
	v_rcp_f32_e32 v215, v215
	v_pk_mul_f32 v[208:209], v[102:103], v[208:209]
	v_pk_mul_f32 v[210:211], v[104:105], v[210:211]
	v_pk_mul_f32 v[212:213], v[94:95], v[212:213]
	v_pk_mul_f32 v[214:215], v[96:97], v[214:215]
	v_pk_mul_f32 v[208:209], v[98:99], v[208:209]
	v_pk_mul_f32 v[210:211], v[100:101], v[210:211]
	v_pk_mul_f32 v[212:213], v[90:91], v[212:213]
	v_pk_mul_f32 v[214:215], v[92:93], v[214:215]
	v_med3_f32 v208, v208, s97, v230
	v_med3_f32 v209, v209, s97, v230
	v_med3_f32 v210, v210, s97, v230
	v_med3_f32 v211, v211, s97, v230
	v_med3_f32 v212, v212, s97, v230
	v_med3_f32 v213, v213, s97, v230
	v_med3_f32 v214, v214, s97, v230
	v_med3_f32 v215, v215, s97, v230
	v_cvt_pk_fp8_f32 v102, v208, v209
	v_cvt_pk_fp8_f32 v103, v212, v213
	v_cvt_pk_fp8_f32 v102, v210, v211 op_sel:[0,0,1]
	v_cvt_pk_fp8_f32 v103, v214, v215 op_sel:[0,0,1]
	v_add_u32_e32 v216, 0x16000, v184
	global_store_dwordx2 v216, v[102:103], s[4:5]
	v_cvt_f32_i32_e32 v86, v86
	v_cvt_f32_i32_e32 v87, v87
	v_cvt_f32_i32_e32 v88, v88
	v_cvt_f32_i32_e32 v89, v89
	v_cvt_f32_i32_e32 v78, v78
	v_cvt_f32_i32_e32 v79, v79
	v_cvt_f32_i32_e32 v80, v80
	v_cvt_f32_i32_e32 v81, v81
	v_cvt_f32_i32_e32 v82, v82
	v_cvt_f32_i32_e32 v83, v83
	v_cvt_f32_i32_e32 v84, v84
	v_cvt_f32_i32_e32 v85, v85
	v_cvt_f32_i32_e32 v74, v74
	v_cvt_f32_i32_e32 v75, v75
	v_cvt_f32_i32_e32 v76, v76
	v_cvt_f32_i32_e32 v77, v77
	v_pk_mul_f32 v[188:189], v[160:161], v[178:179] op_sel:[0,1]
	v_pk_mul_f32 v[190:191], v[162:163], v[178:179] op_sel:[0,1]
	v_pk_mul_f32 v[192:193], v[164:165], v[178:179] op_sel:[0,1]
	v_pk_mul_f32 v[194:195], v[166:167], v[178:179] op_sel:[0,1]
	v_pk_mul_f32 v[196:197], v[168:169], v[178:179] op_sel:[0,1]
	v_pk_mul_f32 v[198:199], v[170:171], v[178:179] op_sel:[0,1]
	v_pk_mul_f32 v[204:205], v[172:173], v[178:179] op_sel:[0,1]
	v_pk_mul_f32 v[206:207], v[174:175], v[178:179] op_sel:[0,1]
	v_pk_mul_f32 v[86:87], v[188:189], v[86:87]
	v_pk_mul_f32 v[88:89], v[190:191], v[88:89]
	v_pk_mul_f32 v[78:79], v[192:193], v[78:79]
	v_pk_mul_f32 v[80:81], v[194:195], v[80:81]
	v_pk_mul_f32 v[82:83], v[196:197], v[82:83]
	v_pk_mul_f32 v[84:85], v[198:199], v[84:85]
	v_pk_mul_f32 v[74:75], v[204:205], v[74:75]
	v_pk_mul_f32 v[76:77], v[206:207], v[76:77]
	v_pk_mul_f32 v[208:209], v[86:87], s[100:101]
	v_pk_mul_f32 v[210:211], v[88:89], s[100:101]
	v_pk_mul_f32 v[212:213], v[78:79], s[100:101]
	v_pk_mul_f32 v[214:215], v[80:81], s[100:101]
	v_exp_f32_e32 v208, v208
	v_exp_f32_e32 v209, v209
	v_exp_f32_e32 v210, v210
	v_exp_f32_e32 v211, v211
	v_exp_f32_e32 v212, v212
	v_exp_f32_e32 v213, v213
	v_exp_f32_e32 v214, v214
	v_exp_f32_e32 v215, v215
	v_pk_add_f32 v[208:209], v[208:209], v[186:187]
	v_pk_add_f32 v[210:211], v[210:211], v[186:187]
	v_pk_add_f32 v[212:213], v[212:213], v[186:187]
	v_pk_add_f32 v[214:215], v[214:215], v[186:187]
	v_rcp_f32_e32 v208, v208
	v_rcp_f32_e32 v209, v209
	v_rcp_f32_e32 v210, v210
	v_rcp_f32_e32 v211, v211
	v_rcp_f32_e32 v212, v212
	v_rcp_f32_e32 v213, v213
	v_rcp_f32_e32 v214, v214
	v_rcp_f32_e32 v215, v215
	v_pk_mul_f32 v[208:209], v[86:87], v[208:209]
	v_pk_mul_f32 v[210:211], v[88:89], v[210:211]
	v_pk_mul_f32 v[212:213], v[78:79], v[212:213]
	v_pk_mul_f32 v[214:215], v[80:81], v[214:215]
	v_pk_mul_f32 v[208:209], v[82:83], v[208:209]
	v_pk_mul_f32 v[210:211], v[84:85], v[210:211]
	v_pk_mul_f32 v[212:213], v[74:75], v[212:213]
	v_pk_mul_f32 v[214:215], v[76:77], v[214:215]
	v_med3_f32 v208, v208, s97, v230
	v_med3_f32 v209, v209, s97, v230
	v_med3_f32 v210, v210, s97, v230
	v_med3_f32 v211, v211, s97, v230
	v_med3_f32 v212, v212, s97, v230
	v_med3_f32 v213, v213, s97, v230
	v_med3_f32 v214, v214, s97, v230
	v_med3_f32 v215, v215, s97, v230
	v_cvt_pk_fp8_f32 v86, v208, v209
	v_cvt_pk_fp8_f32 v87, v212, v213
	v_cvt_pk_fp8_f32 v86, v210, v211 op_sel:[0,0,1]
	v_cvt_pk_fp8_f32 v87, v214, v215 op_sel:[0,0,1]
	v_add_u32_e32 v216, 0x21000, v184
	global_store_dwordx2 v216, v[86:87], s[4:5]
	v_cvt_f32_i32_e32 v70, v70
	v_cvt_f32_i32_e32 v71, v71
	v_cvt_f32_i32_e32 v72, v72
	v_cvt_f32_i32_e32 v73, v73
	v_cvt_f32_i32_e32 v62, v62
	v_cvt_f32_i32_e32 v63, v63
	v_cvt_f32_i32_e32 v64, v64
	v_cvt_f32_i32_e32 v65, v65
	v_cvt_f32_i32_e32 v66, v66
	v_cvt_f32_i32_e32 v67, v67
	v_cvt_f32_i32_e32 v68, v68
	v_cvt_f32_i32_e32 v69, v69
	v_cvt_f32_i32_e32 v58, v58
	v_cvt_f32_i32_e32 v59, v59
	v_cvt_f32_i32_e32 v60, v60
	v_cvt_f32_i32_e32 v61, v61
	v_pk_mul_f32 v[188:189], v[160:161], v[180:181] op_sel_hi:[1,0]
	v_pk_mul_f32 v[190:191], v[162:163], v[180:181] op_sel_hi:[1,0]
	v_pk_mul_f32 v[192:193], v[164:165], v[180:181] op_sel_hi:[1,0]
	v_pk_mul_f32 v[194:195], v[166:167], v[180:181] op_sel_hi:[1,0]
	v_pk_mul_f32 v[196:197], v[168:169], v[180:181] op_sel_hi:[1,0]
	v_pk_mul_f32 v[198:199], v[170:171], v[180:181] op_sel_hi:[1,0]
	v_pk_mul_f32 v[204:205], v[172:173], v[180:181] op_sel_hi:[1,0]
	v_pk_mul_f32 v[206:207], v[174:175], v[180:181] op_sel_hi:[1,0]
	v_pk_mul_f32 v[70:71], v[188:189], v[70:71]
	v_pk_mul_f32 v[72:73], v[190:191], v[72:73]
	v_pk_mul_f32 v[62:63], v[192:193], v[62:63]
	v_pk_mul_f32 v[64:65], v[194:195], v[64:65]
	v_pk_mul_f32 v[66:67], v[196:197], v[66:67]
	v_pk_mul_f32 v[68:69], v[198:199], v[68:69]
	v_pk_mul_f32 v[58:59], v[204:205], v[58:59]
	v_pk_mul_f32 v[60:61], v[206:207], v[60:61]
	v_pk_mul_f32 v[208:209], v[70:71], s[100:101]
	v_pk_mul_f32 v[210:211], v[72:73], s[100:101]
	v_pk_mul_f32 v[212:213], v[62:63], s[100:101]
	v_pk_mul_f32 v[214:215], v[64:65], s[100:101]
	v_exp_f32_e32 v208, v208
	v_exp_f32_e32 v209, v209
	v_exp_f32_e32 v210, v210
	v_exp_f32_e32 v211, v211
	v_exp_f32_e32 v212, v212
	v_exp_f32_e32 v213, v213
	v_exp_f32_e32 v214, v214
	v_exp_f32_e32 v215, v215
	v_pk_add_f32 v[208:209], v[208:209], v[186:187]
	v_pk_add_f32 v[210:211], v[210:211], v[186:187]
	v_pk_add_f32 v[212:213], v[212:213], v[186:187]
	v_pk_add_f32 v[214:215], v[214:215], v[186:187]
	v_rcp_f32_e32 v208, v208
	v_rcp_f32_e32 v209, v209
	v_rcp_f32_e32 v210, v210
	v_rcp_f32_e32 v211, v211
	v_rcp_f32_e32 v212, v212
	v_rcp_f32_e32 v213, v213
	v_rcp_f32_e32 v214, v214
	v_rcp_f32_e32 v215, v215
	v_pk_mul_f32 v[208:209], v[70:71], v[208:209]
	v_pk_mul_f32 v[210:211], v[72:73], v[210:211]
	v_pk_mul_f32 v[212:213], v[62:63], v[212:213]
	v_pk_mul_f32 v[214:215], v[64:65], v[214:215]
	v_pk_mul_f32 v[208:209], v[66:67], v[208:209]
	v_pk_mul_f32 v[210:211], v[68:69], v[210:211]
	v_pk_mul_f32 v[212:213], v[58:59], v[212:213]
	v_pk_mul_f32 v[214:215], v[60:61], v[214:215]
	v_med3_f32 v208, v208, s97, v230
	v_med3_f32 v209, v209, s97, v230
	v_med3_f32 v210, v210, s97, v230
	v_med3_f32 v211, v211, s97, v230
	v_med3_f32 v212, v212, s97, v230
	v_med3_f32 v213, v213, s97, v230
	v_med3_f32 v214, v214, s97, v230
	v_med3_f32 v215, v215, s97, v230
	v_cvt_pk_fp8_f32 v70, v208, v209
	v_cvt_pk_fp8_f32 v71, v212, v213
	v_cvt_pk_fp8_f32 v70, v210, v211 op_sel:[0,0,1]
	v_cvt_pk_fp8_f32 v71, v214, v215 op_sel:[0,0,1]
	v_add_u32_e32 v216, 0x58000, v184
	global_store_dwordx2 v216, v[70:71], s[4:5]
	v_cvt_f32_i32_e32 v54, v54
	v_cvt_f32_i32_e32 v55, v55
	v_cvt_f32_i32_e32 v56, v56
	v_cvt_f32_i32_e32 v57, v57
	v_cvt_f32_i32_e32 v42, v42
	v_cvt_f32_i32_e32 v43, v43
	v_cvt_f32_i32_e32 v44, v44
	v_cvt_f32_i32_e32 v45, v45
	v_cvt_f32_i32_e32 v50, v50
	v_cvt_f32_i32_e32 v51, v51
	v_cvt_f32_i32_e32 v52, v52
	v_cvt_f32_i32_e32 v53, v53
	v_cvt_f32_i32_e32 v38, v38
	v_cvt_f32_i32_e32 v39, v39
	v_cvt_f32_i32_e32 v40, v40
	v_cvt_f32_i32_e32 v41, v41
	v_pk_mul_f32 v[188:189], v[160:161], v[180:181] op_sel:[0,1]
	v_pk_mul_f32 v[190:191], v[162:163], v[180:181] op_sel:[0,1]
	v_pk_mul_f32 v[192:193], v[164:165], v[180:181] op_sel:[0,1]
	v_pk_mul_f32 v[194:195], v[166:167], v[180:181] op_sel:[0,1]
	v_pk_mul_f32 v[196:197], v[168:169], v[180:181] op_sel:[0,1]
	v_pk_mul_f32 v[198:199], v[170:171], v[180:181] op_sel:[0,1]
	v_pk_mul_f32 v[204:205], v[172:173], v[180:181] op_sel:[0,1]
	v_pk_mul_f32 v[206:207], v[174:175], v[180:181] op_sel:[0,1]
	v_pk_mul_f32 v[54:55], v[188:189], v[54:55]
	v_pk_mul_f32 v[56:57], v[190:191], v[56:57]
	v_pk_mul_f32 v[42:43], v[192:193], v[42:43]
	v_pk_mul_f32 v[44:45], v[194:195], v[44:45]
	v_pk_mul_f32 v[50:51], v[196:197], v[50:51]
	v_pk_mul_f32 v[52:53], v[198:199], v[52:53]
	v_pk_mul_f32 v[38:39], v[204:205], v[38:39]
	v_pk_mul_f32 v[40:41], v[206:207], v[40:41]
	v_pk_mul_f32 v[208:209], v[54:55], s[100:101]
	v_pk_mul_f32 v[210:211], v[56:57], s[100:101]
	v_pk_mul_f32 v[212:213], v[42:43], s[100:101]
	v_pk_mul_f32 v[214:215], v[44:45], s[100:101]
	v_exp_f32_e32 v208, v208
	v_exp_f32_e32 v209, v209
	v_exp_f32_e32 v210, v210
	v_exp_f32_e32 v211, v211
	v_exp_f32_e32 v212, v212
	v_exp_f32_e32 v213, v213
	v_exp_f32_e32 v214, v214
	v_exp_f32_e32 v215, v215
	v_pk_add_f32 v[208:209], v[208:209], v[186:187]
	v_pk_add_f32 v[210:211], v[210:211], v[186:187]
	v_pk_add_f32 v[212:213], v[212:213], v[186:187]
	v_pk_add_f32 v[214:215], v[214:215], v[186:187]
	v_rcp_f32_e32 v208, v208
	v_rcp_f32_e32 v209, v209
	v_rcp_f32_e32 v210, v210
	v_rcp_f32_e32 v211, v211
	v_rcp_f32_e32 v212, v212
	v_rcp_f32_e32 v213, v213
	v_rcp_f32_e32 v214, v214
	v_rcp_f32_e32 v215, v215
	v_pk_mul_f32 v[208:209], v[54:55], v[208:209]
	v_pk_mul_f32 v[210:211], v[56:57], v[210:211]
	v_pk_mul_f32 v[212:213], v[42:43], v[212:213]
	v_pk_mul_f32 v[214:215], v[44:45], v[214:215]
	v_pk_mul_f32 v[208:209], v[50:51], v[208:209]
	v_pk_mul_f32 v[210:211], v[52:53], v[210:211]
	v_pk_mul_f32 v[212:213], v[38:39], v[212:213]
	v_pk_mul_f32 v[214:215], v[40:41], v[214:215]
	v_med3_f32 v208, v208, s97, v230
	v_med3_f32 v209, v209, s97, v230
	v_med3_f32 v210, v210, s97, v230
	v_med3_f32 v211, v211, s97, v230
	v_med3_f32 v212, v212, s97, v230
	v_med3_f32 v213, v213, s97, v230
	v_med3_f32 v214, v214, s97, v230
	v_med3_f32 v215, v215, s97, v230
	v_cvt_pk_fp8_f32 v54, v208, v209
	v_cvt_pk_fp8_f32 v55, v212, v213
	v_cvt_pk_fp8_f32 v54, v210, v211 op_sel:[0,0,1]
	v_cvt_pk_fp8_f32 v55, v214, v215 op_sel:[0,0,1]
	v_add_u32_e32 v216, 0x63000, v184
	global_store_dwordx2 v216, v[54:55], s[4:5]
	v_cvt_f32_i32_e32 v30, v30
	v_cvt_f32_i32_e32 v31, v31
	v_cvt_f32_i32_e32 v32, v32
	v_cvt_f32_i32_e32 v33, v33
	v_cvt_f32_i32_e32 v22, v22
	v_cvt_f32_i32_e32 v23, v23
	v_cvt_f32_i32_e32 v24, v24
	v_cvt_f32_i32_e32 v25, v25
	v_cvt_f32_i32_e32 v26, v26
	v_cvt_f32_i32_e32 v27, v27
	v_cvt_f32_i32_e32 v28, v28
	v_cvt_f32_i32_e32 v29, v29
	v_cvt_f32_i32_e32 v18, v18
	v_cvt_f32_i32_e32 v19, v19
	v_cvt_f32_i32_e32 v20, v20
	v_cvt_f32_i32_e32 v21, v21
	v_pk_mul_f32 v[188:189], v[160:161], v[182:183] op_sel_hi:[1,0]
	v_pk_mul_f32 v[190:191], v[162:163], v[182:183] op_sel_hi:[1,0]
	v_pk_mul_f32 v[192:193], v[164:165], v[182:183] op_sel_hi:[1,0]
	v_pk_mul_f32 v[194:195], v[166:167], v[182:183] op_sel_hi:[1,0]
	v_pk_mul_f32 v[196:197], v[168:169], v[182:183] op_sel_hi:[1,0]
	v_pk_mul_f32 v[198:199], v[170:171], v[182:183] op_sel_hi:[1,0]
	v_pk_mul_f32 v[204:205], v[172:173], v[182:183] op_sel_hi:[1,0]
	v_pk_mul_f32 v[206:207], v[174:175], v[182:183] op_sel_hi:[1,0]
	v_pk_mul_f32 v[30:31], v[188:189], v[30:31]
	v_pk_mul_f32 v[32:33], v[190:191], v[32:33]
	v_pk_mul_f32 v[22:23], v[192:193], v[22:23]
	v_pk_mul_f32 v[24:25], v[194:195], v[24:25]
	v_pk_mul_f32 v[26:27], v[196:197], v[26:27]
	v_pk_mul_f32 v[28:29], v[198:199], v[28:29]
	v_pk_mul_f32 v[18:19], v[204:205], v[18:19]
	v_pk_mul_f32 v[20:21], v[206:207], v[20:21]
	v_pk_mul_f32 v[208:209], v[30:31], s[100:101]
	v_pk_mul_f32 v[210:211], v[32:33], s[100:101]
	v_pk_mul_f32 v[212:213], v[22:23], s[100:101]
	v_pk_mul_f32 v[214:215], v[24:25], s[100:101]
	v_exp_f32_e32 v208, v208
	v_exp_f32_e32 v209, v209
	v_exp_f32_e32 v210, v210
	v_exp_f32_e32 v211, v211
	v_exp_f32_e32 v212, v212
	v_exp_f32_e32 v213, v213
	v_exp_f32_e32 v214, v214
	v_exp_f32_e32 v215, v215
	v_pk_add_f32 v[208:209], v[208:209], v[186:187]
	v_pk_add_f32 v[210:211], v[210:211], v[186:187]
	v_pk_add_f32 v[212:213], v[212:213], v[186:187]
	v_pk_add_f32 v[214:215], v[214:215], v[186:187]
	v_rcp_f32_e32 v208, v208
	v_rcp_f32_e32 v209, v209
	v_rcp_f32_e32 v210, v210
	v_rcp_f32_e32 v211, v211
	v_rcp_f32_e32 v212, v212
	v_rcp_f32_e32 v213, v213
	v_rcp_f32_e32 v214, v214
	v_rcp_f32_e32 v215, v215
	v_pk_mul_f32 v[208:209], v[30:31], v[208:209]
	v_pk_mul_f32 v[210:211], v[32:33], v[210:211]
	v_pk_mul_f32 v[212:213], v[22:23], v[212:213]
	v_pk_mul_f32 v[214:215], v[24:25], v[214:215]
	v_pk_mul_f32 v[208:209], v[26:27], v[208:209]
	v_pk_mul_f32 v[210:211], v[28:29], v[210:211]
	v_pk_mul_f32 v[212:213], v[18:19], v[212:213]
	v_pk_mul_f32 v[214:215], v[20:21], v[214:215]
	v_med3_f32 v208, v208, s97, v230
	v_med3_f32 v209, v209, s97, v230
	v_med3_f32 v210, v210, s97, v230
	v_med3_f32 v211, v211, s97, v230
	v_med3_f32 v212, v212, s97, v230
	v_med3_f32 v213, v213, s97, v230
	v_med3_f32 v214, v214, s97, v230
	v_med3_f32 v215, v215, s97, v230
	v_cvt_pk_fp8_f32 v30, v208, v209
	v_cvt_pk_fp8_f32 v31, v212, v213
	v_cvt_pk_fp8_f32 v30, v210, v211 op_sel:[0,0,1]
	v_cvt_pk_fp8_f32 v31, v214, v215 op_sel:[0,0,1]
	v_add_u32_e32 v216, 0x6e000, v184
	global_store_dwordx2 v216, v[30:31], s[4:5]
	v_cvt_f32_i32_e32 v10, v10
	v_cvt_f32_i32_e32 v11, v11
	v_cvt_f32_i32_e32 v12, v12
	v_cvt_f32_i32_e32 v13, v13
	v_cvt_f32_i32_e32 v2, v2
	v_cvt_f32_i32_e32 v3, v3
	v_cvt_f32_i32_e32 v4, v4
	v_cvt_f32_i32_e32 v5, v5
	v_cvt_f32_i32_e32 v14, v14
	v_cvt_f32_i32_e32 v15, v15
	v_cvt_f32_i32_e32 v16, v16
	v_cvt_f32_i32_e32 v17, v17
	v_cvt_f32_i32_e32 v6, v6
	v_cvt_f32_i32_e32 v7, v7
	v_cvt_f32_i32_e32 v8, v8
	v_cvt_f32_i32_e32 v9, v9
	v_pk_mul_f32 v[188:189], v[160:161], v[182:183] op_sel:[0,1]
	v_pk_mul_f32 v[190:191], v[162:163], v[182:183] op_sel:[0,1]
	v_pk_mul_f32 v[192:193], v[164:165], v[182:183] op_sel:[0,1]
	v_pk_mul_f32 v[194:195], v[166:167], v[182:183] op_sel:[0,1]
	v_pk_mul_f32 v[196:197], v[168:169], v[182:183] op_sel:[0,1]
	v_pk_mul_f32 v[198:199], v[170:171], v[182:183] op_sel:[0,1]
	v_pk_mul_f32 v[204:205], v[172:173], v[182:183] op_sel:[0,1]
	v_pk_mul_f32 v[206:207], v[174:175], v[182:183] op_sel:[0,1]
	v_pk_mul_f32 v[10:11], v[188:189], v[10:11]
	v_pk_mul_f32 v[12:13], v[190:191], v[12:13]
	v_pk_mul_f32 v[2:3], v[192:193], v[2:3]
	v_pk_mul_f32 v[4:5], v[194:195], v[4:5]
	v_pk_mul_f32 v[14:15], v[196:197], v[14:15]
	v_pk_mul_f32 v[16:17], v[198:199], v[16:17]
	v_pk_mul_f32 v[6:7], v[204:205], v[6:7]
	v_pk_mul_f32 v[8:9], v[206:207], v[8:9]
	v_pk_mul_f32 v[208:209], v[10:11], s[100:101]
	v_pk_mul_f32 v[210:211], v[12:13], s[100:101]
	v_pk_mul_f32 v[212:213], v[2:3], s[100:101]
	v_pk_mul_f32 v[214:215], v[4:5], s[100:101]
	v_exp_f32_e32 v208, v208
	v_exp_f32_e32 v209, v209
	v_exp_f32_e32 v210, v210
	v_exp_f32_e32 v211, v211
	v_exp_f32_e32 v212, v212
	v_exp_f32_e32 v213, v213
	v_exp_f32_e32 v214, v214
	v_exp_f32_e32 v215, v215
	v_pk_add_f32 v[208:209], v[208:209], v[186:187]
	v_pk_add_f32 v[210:211], v[210:211], v[186:187]
	v_pk_add_f32 v[212:213], v[212:213], v[186:187]
	v_pk_add_f32 v[214:215], v[214:215], v[186:187]
	v_rcp_f32_e32 v208, v208
	v_rcp_f32_e32 v209, v209
	v_rcp_f32_e32 v210, v210
	v_rcp_f32_e32 v211, v211
	v_rcp_f32_e32 v212, v212
	v_rcp_f32_e32 v213, v213
	v_rcp_f32_e32 v214, v214
	v_rcp_f32_e32 v215, v215
	v_pk_mul_f32 v[208:209], v[10:11], v[208:209]
	v_pk_mul_f32 v[210:211], v[12:13], v[210:211]
	v_pk_mul_f32 v[212:213], v[2:3], v[212:213]
	v_pk_mul_f32 v[214:215], v[4:5], v[214:215]
	v_pk_mul_f32 v[208:209], v[14:15], v[208:209]
	v_pk_mul_f32 v[210:211], v[16:17], v[210:211]
	v_pk_mul_f32 v[212:213], v[6:7], v[212:213]
	v_pk_mul_f32 v[214:215], v[8:9], v[214:215]
	v_med3_f32 v208, v208, s97, v230
	v_med3_f32 v209, v209, s97, v230
	v_med3_f32 v210, v210, s97, v230
	v_med3_f32 v211, v211, s97, v230
	v_med3_f32 v212, v212, s97, v230
	v_med3_f32 v213, v213, s97, v230
	v_med3_f32 v214, v214, s97, v230
	v_med3_f32 v215, v215, s97, v230
	v_cvt_pk_fp8_f32 v10, v208, v209
	v_cvt_pk_fp8_f32 v11, v212, v213
	v_cvt_pk_fp8_f32 v10, v210, v211 op_sel:[0,0,1]
	v_cvt_pk_fp8_f32 v11, v214, v215 op_sel:[0,0,1]
	v_add_u32_e32 v216, 0x79000, v184
	global_store_dwordx2 v216, v[10:11], s[4:5]
	v_readlane_b32 s58, v251, 51
	v_readlane_b32 s59, v251, 52
	s_mov_b32 s78, 0xf800000
	s_andn2_b64 vcc, exec, s[30:31]
	s_mov_b64 s[34:35], -1
	s_cbranch_vccnz .LBB0_1374
	s_andn2_b64 vcc, exec, s[0:1]
	s_cbranch_vccnz .LBB0_1373
	s_barrier
	s_branch .LBB0_1373

	.amdhsa_kernel _Z9trunk_fwd4Args
		.amdhsa_group_segment_fixed_size 0
		.amdhsa_private_segment_fixed_size 0
		.amdhsa_kernarg_size 432
		.amdhsa_user_sgpr_count 2
		.amdhsa_user_sgpr_dispatch_ptr 0
		.amdhsa_user_sgpr_queue_ptr 0
		.amdhsa_user_sgpr_kernarg_segment_ptr 1
		.amdhsa_user_sgpr_dispatch_id 0
		.amdhsa_user_sgpr_kernarg_preload_length 0
		.amdhsa_user_sgpr_kernarg_preload_offset 0
		.amdhsa_user_sgpr_private_segment_size 0
		.amdhsa_uses_dynamic_stack 0
		.amdhsa_enable_private_segment 0
		.amdhsa_system_sgpr_workgroup_id_x 1
		.amdhsa_system_sgpr_workgroup_id_y 0
		.amdhsa_system_sgpr_workgroup_id_z 0
		.amdhsa_system_sgpr_workgroup_info 0
		.amdhsa_system_vgpr_workitem_id 0
		.amdhsa_next_free_vgpr 256
		.amdhsa_next_free_sgpr 102
		.amdhsa_accum_offset 256
		.amdhsa_reserve_vcc 1
		.amdhsa_float_round_mode_32 0
		.amdhsa_float_round_mode_16_64 0
		.amdhsa_float_denorm_mode_32 3
		.amdhsa_float_denorm_mode_16_64 3
		.amdhsa_dx10_clamp 1
		.amdhsa_ieee_mode 1
		.amdhsa_fp16_overflow 0
		.amdhsa_tg_split 0
		.amdhsa_exception_fp_ieee_invalid_op 0
		.amdhsa_exception_fp_denorm_src 0
		.amdhsa_exception_fp_ieee_div_zero 0
		.amdhsa_exception_fp_ieee_overflow 0
		.amdhsa_exception_fp_ieee_underflow 0
		.amdhsa_exception_fp_ieee_inexact 0
		.amdhsa_exception_int_div_zero 0
	.end_amdhsa_kernel

amdhsa.kernels:
  - .agpr_count:     0
    .args:
      - .offset:         0
        .size:           176
        .value_kind:     by_value
      - .offset:         176
        .size:           4
        .value_kind:     hidden_block_count_x
      - .offset:         180
        .size:           4
        .value_kind:     hidden_block_count_y
      - .offset:         184
        .size:           4
        .value_kind:     hidden_block_count_z
      - .offset:         188
        .size:           2
        .value_kind:     hidden_group_size_x
      - .offset:         190
        .size:           2
        .value_kind:     hidden_group_size_y
      - .offset:         192
        .size:           2
        .value_kind:     hidden_group_size_z
      - .offset:         194
        .size:           2
        .value_kind:     hidden_remainder_x
      - .offset:         196
        .size:           2
        .value_kind:     hidden_remainder_y
      - .offset:         198
        .size:           2
        .value_kind:     hidden_remainder_z
      - .offset:         216
        .size:           8
        .value_kind:     hidden_global_offset_x
      - .offset:         224
        .size:           8
        .value_kind:     hidden_global_offset_y
      - .offset:         232
        .size:           8
        .value_kind:     hidden_global_offset_z
      - .offset:         240
        .size:           2
        .value_kind:     hidden_grid_dims
      - .offset:         296
        .size:           4
        .value_kind:     hidden_dynamic_lds_size
    .group_segment_fixed_size: 0
    .kernarg_segment_align: 8
    .kernarg_segment_size: 432
    .language:       OpenCL C
    .language_version:
      - 2
      - 0
    .max_flat_workgroup_size: 512
    .name:           _Z9trunk_fwd4Args
    .private_segment_fixed_size: 0
    .sgpr_count:     108
    .sgpr_spill_count: 275
    .symbol:         _Z9trunk_fwd4Args.kd
    .uniform_work_group_size: 1
    .uses_dynamic_stack: false
    .vgpr_count:     256
    .vgpr_spill_count: 0
    .wavefront_size: 64
